# light-tile K-loops: A tile via ordinary loads, waves 4-7 prefetch weights two tiles ahead using their idle accumulators
# baseline (speedup 1.0000x reference)
; #define G_DMA_A(buf, t, i_) __builtin_amdgcn_raw_ptr_buffer_load_lds(ra, (LAS void*)(lds + (buf) * 65536 + a_wu + (i_) * 8192), 16, ao##i_, (unsigned)(t) * 128u, 0, 0)
; #define G_ISSUE_B(t) do { const unsigned so_ = (unsigned)(t) * 64u * ldbB; _Pragma("unroll") for (int i_ = 0; i_ < 8; ++i_) sb[i_] = __builtin_bit_cast(f32x4, __builtin_amdgcn_raw_buffer_load_b128(rb, bo, so_ + (unsigned)i_ * ldbB, 0)); } while (0)
; #define G_RETIRE() asm volatile("s_waitcnt vmcnt(0)" : "+v"(sb[0]), "+v"(sb[1]), "+v"(sb[2]), "+v"(sb[3]), "+v"(sb[4]), "+v"(sb[5]), "+v"(sb[6]), "+v"(sb[7]) :: "memory")
; #define G_WRITE_B(buf) do { LAS unsigned char* d_ = lds + (buf) * 65536; \
;         _Pragma("unroll") for (int j_ = 0; j_ < 4; ++j_) { u32x4 w_; w_.x = cvtpk(sb[0][j_], sb[1][j_]); w_.y = cvtpk(sb[2][j_], sb[3][j_]); w_.z = cvtpk(sb[4][j_], sb[5][j_]); w_.w = cvtpk(sb[6][j_], sb[7][j_]); \
;             *(LAS u32x4*)(d_ + 32768 + T.b_w + ((T.b_rot + 64u * j_) & 255u)) = w_; } } while (0)
; __device__ __forceinline__ void gemm_kloop_light(f32x4 (&acc)[8][4], LAS unsigned char* lds, const GemmT& T, ...
;     ...
;     G_ISSUE_B(0); G_DMA_A(0, 0, 0); G_DMA_A(0, 0, 1); G_DMA_A(0, 0, 2); G_DMA_A(0, 0, 3); G_RETIRE(); G_WRITE_B(0);
;     if (nt > 1) G_ISSUE_B(1);
;     G_BAR();
; __device__ __forceinline__ void phase_moe_gu(const Ptrs& p, LAS unsigned char* lds) {
;     ...
;         GemmT T; T.init();
;         const int* list = (const int*)(p.ws + OFF_LIST) + (size_t)mu.e * NTOK; const int i0 = mu.mt * 256, n0 = mu.nt * 128;
;         unsigned ao[4];
; #pragma unroll
;         for (int i = 0; i < 4; ++i) { const int r = i0 + T.aR + 64 * i; const int tok = (r < mu.cnt) ? (list[r] >> 2) : 0; ao[i] = (unsigned)((tok * D + T.aC) * 2); }
;         const float* wsel = ((__builtin_amdgcn_readfirstlane(T.b_p) & 1) ? p.w_up : p.w_gate) + (size_t)mu.e * D * D + n0;
;         const unsigned bo = (unsigned)((T.b_k * D + T.b_gucol) * 4);
;         f32x4 acc[8][4]; acc_zero(acc);
;         const int mlim = __builtin_amdgcn_readfirstlane(T.wr) ? 0 : ((mu.cnt - i0 + 15) >> 4);
;         if (mu.light) gemm_kloop_light(acc, lds, T, mk_rsrc(h2), ao[0], ao[1], ao[2], ao[3], mk_rsrc(wsel), bo, D * 4u, D / 64, mlim);
;         else gemm_kloop(acc, lds, T, mk_rsrc(h2), ao[0], ao[1], ao[2], ao[3], mk_rsrc(wsel), bo, D * 4u, D / 64);
.LBB0_1163:
	s_andn2_b64 vcc, exec, s[0:1]
	s_mov_b64 s[0:1], -1
	s_cbranch_vccnz .LBB0_1005
	s_ashr_i32 s43, s42, 31
	s_lshl_b64 s[0:1], s[42:43], 15
	v_mov_b32_e32 v3, v0
	s_add_u32 s0, s52, s0
	s_addc_u32 s1, s53, s1
	v_bfe_u32 v4, v3, 2, 4
	s_lshl_b32 s2, s86, 8
	v_ashrrev_i32_e32 v10, 7, v3
	v_or_b32_e32 v4, s2, v4
	v_lshl_add_u32 v4, v10, 4, v4
	v_cmp_gt_i32_e32 vcc, s87, v4
	v_mov_b32_e32 v6, 0
	v_ashrrev_i32_e32 v5, 31, v4
	v_mov_b32_e32 v7, 0
	v_mov_b32_e32 v8, 0
	v_mov_b32_e32 v9, 0
	v_lshl_add_u64 v[12:13], v[4:5], 2, s[0:1]
	s_and_saveexec_b64 s[4:5], vcc
	global_load_dword v7, v[12:13], off
	s_or_b64 exec, exec, s[4:5]
	v_add_u32_e32 v11, 64, v4
	v_cmp_gt_i32_e32 vcc, s87, v11
	s_and_saveexec_b64 s[4:5], vcc
	global_load_dword v6, v[12:13], off offset:256
	s_or_b64 exec, exec, s[4:5]
	v_add_u32_e32 v11, 0x80, v4
	v_cmp_gt_i32_e32 vcc, s87, v11
	s_and_saveexec_b64 s[4:5], vcc
	global_load_dword v9, v[12:13], off offset:512
	s_or_b64 exec, exec, s[4:5]
	v_add_u32_e32 v11, 0xc0, v4
	v_cmp_gt_i32_e32 vcc, s87, v11
	s_and_saveexec_b64 s[4:5], vcc
	global_load_dword v8, v[12:13], off offset:768
	s_or_b64 exec, exec, s[4:5]
	v_ashrrev_i32_e32 v5, 6, v3
	v_and_b32_e32 v11, 1, v5
	s_lshl_b32 s0, s85, 7
	v_readfirstlane_b32 s1, v11
	v_readlane_b32 s4, v246, 0
	s_bitcmp0_b32 s1, 0
	v_readlane_b32 s5, v246, 1
	s_cselect_b32 s1, s49, s5
	s_cselect_b32 s3, s48, s4
	s_lshl_b64 s[4:5], s[42:43], 24
	v_readlane_b32 s6, v246, 2
	s_add_u32 s3, s3, s4
	v_and_b32_e32 v4, 63, v3
	s_addc_u32 s6, s1, s5
	s_ashr_i32 s1, s0, 31
	v_lshrrev_b32_e32 v12, 5, v4
	v_bfe_u32 v13, v3, 1, 2
	s_lshl_b64 s[4:5], s[0:1], 2
	v_lshl_or_b32 v10, v10, 1, v12
	v_bfe_u32 v12, v3, 3, 2
	v_and_b32_e32 v14, 1, v3
	v_lshlrev_b32_e32 v15, 5, v13
	s_add_u32 s24, s3, s4
	v_lshl_or_b32 v15, v12, 7, v15
	v_lshlrev_b32_e32 v16, 16, v10
	v_lshlrev_b32_e32 v17, 4, v14
	s_addc_u32 s1, s6, s5
	v_or3_b32 v225, v15, v17, v16
	s_and_b32 s25, s1, 0xffff
	s_movk_i32 s1, 0x2000
	buffer_load_dwordx4 v[114:117], v225, s[24:27], 0 offen
	buffer_load_dwordx4 v[118:121], v225, s[24:27], s66 offen
	s_mov_b32 s3, 0x8000
	buffer_load_dwordx4 v[126:129], v225, s[24:27], s1 offen
	buffer_load_dwordx4 v[122:125], v225, s[24:27], s3 offen
	s_movk_i32 s1, 0x4000
	s_mov_b32 s3, 0xa000
	buffer_load_dwordx4 v[130:133], v225, s[24:27], s1 offen
	buffer_load_dwordx4 v[134:137], v225, s[24:27], s3 offen
	s_mov_b32 s1, 0xc000
	s_mov_b32 s3, 0xe000
	buffer_load_dwordx4 v[142:145], v225, s[24:27], s1 offen
	buffer_load_dwordx4 v[146:149], v225, s[24:27], s3 offen
	s_waitcnt vmcnt(8)
	v_lshlrev_b32_e32 v7, 10, v7
	v_and_b32_e32 v7, 0xfffff000, v7
	v_lshlrev_b32_e32 v6, 10, v6
	v_and_b32_e32 v6, 0xfffff000, v6
	v_lshlrev_b32_e32 v9, 10, v9
	v_and_b32_e32 v9, 0xfffff000, v9
	v_lshlrev_b32_e32 v8, 10, v8
	v_and_b32_e32 v8, 0xfffff000, v8
	v_lshlrev_b32_e32 v17, 4, v3
	v_lshlrev_b32_e32 v15, 6, v11
	v_and_b32_e32 v16, 32, v3
	v_and_b32_e32 v17, 48, v17
	v_bitop3_b32 v15, v17, v15, v16 bitop3:0xde
	v_or_b32_e32 v221, v9, v15
	v_lshlrev_b32_e32 v9, 2, v12
	v_lshlrev_b32_e32 v11, 1, v11
	v_or3_b32 v9, v9, v11, v14
	v_lshlrev_b32_e32 v11, 2, v3
	v_and_b32_e32 v12, 0xfffffc00, v11
	v_lshl_add_u32 v9, v9, 11, v12
	v_lshlrev_b32_e32 v12, 8, v13
	v_lshlrev_b32_e32 v10, 4, v10
	v_and_or_b32 v10, v10, 48, v12
	v_lshlrev_b32_e32 v12, 3, v3
	v_or_b32_e32 v223, v7, v15
	v_and_b32_e32 v7, 15, v3
	v_and_b32_e32 v12, 32, v12
	v_or_b32_e32 v222, v6, v15
	v_ashrrev_i32_e32 v6, 8, v3
	v_bitop3_b32 v219, v9, v10, v12 bitop3:0xf6
	v_lshlrev_b32_e32 v7, 6, v7
	v_and_b32_e32 v3, 48, v3
	v_and_b32_e32 v10, 32, v11
	v_or_b32_e32 v9, v7, v3
	v_bitop3_b32 v3, v7, v10, v3 bitop3:0x36
	v_lshlrev_b32_e32 v11, 13, v5
	v_lshlrev_b32_e32 v220, 6, v14
	v_lshlrev_b32_e32 v4, 4, v4
	v_lshlrev_b32_e32 v7, 14, v6
	v_and_or_b32 v226, v11, s66, v3
	v_cmp_eq_u32_e32 vcc, 0, v215
	v_add_u32_e32 v227, 0, v219
	v_add_u32_e32 v3, 0xc0, v220
	v_or_b32_e32 v224, v8, v15
	v_lshl_or_b32 v229, v5, 10, v4
	v_bitop3_b32 v216, v9, v7, v10 bitop3:0xde
	v_or_b32_e32 v217, 0x8000, v226
	v_readfirstlane_b32 s1, v6
	s_and_b64 vcc, exec, vcc
	v_add_u32_e32 v228, v227, v220
	v_and_b32_e32 v218, 0xc0, v3
	v_readlane_b32 s7, v246, 3
	v_readlane_b32 s8, v246, 4
	v_readlane_b32 s9, v246, 5
	v_readlane_b32 s10, v246, 6
	v_readlane_b32 s11, v246, 7
	s_cbranch_vccnz .LBB0_1263
	s_sub_i32 s3, s87, s2
	s_mov_b32 s99, s3
	v_readfirstlane_b32 s100, v0
	s_nop 3
	s_lshr_b32 s100, s100, 7
	s_lshl_b32 s100, s100, 4
	s_add_i32 s3, s3, 15
	s_ashr_i32 s3, s3, 4
	s_cmp_eq_u32 s1, 0
	s_cselect_b32 s1, s3, 0
	v_readfirstlane_b32 s3, v229
	s_and_b32 s3, s3, 0xfffffc00
	s_add_i32 s3, s3, 0
	s_mov_b32 s38, s26
	s_mov_b32 s39, s27
	s_mov_b32 m0, s3
	s_waitcnt vmcnt(6)
	v_mov_b64_e32 v[4:5], v[118:119]
	buffer_load_dwordx4 v223, s[36:39], 0 offen lds
	s_add_i32 m0, s3, 0x2000
	s_waitcnt vmcnt(3)
	v_mov_b64_e32 v[8:9], v[134:135]
	buffer_load_dwordx4 v222, s[36:39], 0 offen lds
	s_add_i32 m0, s3, 0x4000
	v_mov_b64_e32 v[12:13], v[114:115]
	buffer_load_dwordx4 v221, s[36:39], 0 offen lds
	s_add_i32 m0, s3, 0x6000
	s_waitcnt vmcnt(3)
	v_mov_b64_e32 v[16:17], v[146:147]
	v_mov_b64_e32 v[20:21], v[130:131]
	v_mov_b64_e32 v[24:25], v[122:123]
	v_mov_b64_e32 v[28:29], v[142:143]
	v_mov_b64_e32 v[32:33], v[126:127]
	buffer_load_dwordx4 v224, s[36:39], 0 offen lds
	v_mov_b64_e32 v[6:7], v[120:121]
	v_mov_b64_e32 v[10:11], v[136:137]
	v_mov_b64_e32 v[14:15], v[116:117]
	v_mov_b64_e32 v[18:19], v[148:149]
	v_mov_b64_e32 v[22:23], v[132:133]
	v_mov_b64_e32 v[26:27], v[124:125]
	v_mov_b64_e32 v[30:31], v[144:145]
	v_mov_b64_e32 v[34:35], v[128:129]
	s_waitcnt vmcnt(0)
	s_movk_i32 s101, 0x80
	s_cmp_le_i32 s99, s100
	s_cbranch_scc1 .Lmy_rcgP0
	buffer_load_dwordx4 v[236:239], v223, s[36:39], s101 offen
; #define G_DMA_A(buf, t, i_) __builtin_amdgcn_raw_ptr_buffer_load_lds(ra, (LAS void*)(lds + (buf) * 65536 + a_wu + (i_) * 8192), 16, ao##i_, (unsigned)(t) * 128u, 0, 0)
; #define G_ISSUE_B(t) do { const unsigned so_ = (unsigned)(t) * 64u * ldbB; _Pragma("unroll") for (int i_ = 0; i_ < 8; ++i_) sb[i_] = __builtin_bit_cast(f32x4, __builtin_amdgcn_raw_buffer_load_b128(rb, bo, so_ + (unsigned)i_ * ldbB, 0)); } while (0)
; #define G_RETIRE() asm volatile("s_waitcnt vmcnt(0)" : "+v"(sb[0]), "+v"(sb[1]), "+v"(sb[2]), "+v"(sb[3]), "+v"(sb[4]), "+v"(sb[5]), "+v"(sb[6]), "+v"(sb[7]) :: "memory")
; #define G_WRITE_B(buf) do { LAS unsigned char* d_ = lds + (buf) * 65536; \
;         _Pragma("unroll") for (int j_ = 0; j_ < 4; ++j_) { u32x4 w_; w_.x = cvtpk(sb[0][j_], sb[1][j_]); w_.y = cvtpk(sb[2][j_], sb[3][j_]); w_.z = cvtpk(sb[4][j_], sb[5][j_]); w_.w = cvtpk(sb[6][j_], sb[7][j_]); \
;             *(LAS u32x4*)(d_ + 32768 + T.b_w + ((T.b_rot + 64u * j_) & 255u)) = w_; } } while (0)
; #define G_BAR() do { asm volatile("s_waitcnt lgkmcnt(0)" ::: "memory"); __builtin_amdgcn_s_barrier(); asm volatile("" ::: "memory"); } while (0)
; #define G_DMA_A(buf, t, i_) __builtin_amdgcn_raw_ptr_buffer_load_lds(ra, (LAS void*)(lds + (buf) * 65536 + a_wu + (i_) * 8192), 16, ao##i_, (unsigned)(t) * 128u, 0, 0)
; #define G_ISSUE_B(t) do { const unsigned so_ = (unsigned)(t) * 64u * ldbB; _Pragma("unroll") for (int i_ = 0; i_ < 8; ++i_) sb[i_] = __builtin_bit_cast(f32x4, __builtin_amdgcn_raw_buffer_load_b128(rb, bo, so_ + (unsigned)i_ * ldbB, 0)); } while (0)
; #define G_RETIRE() asm volatile("s_waitcnt vmcnt(0)" : "+v"(sb[0]), "+v"(sb[1]), "+v"(sb[2]), "+v"(sb[3]), "+v"(sb[4]), "+v"(sb[5]), "+v"(sb[6]), "+v"(sb[7]) :: "memory")
; __device__ __forceinline__ void gemm_kloop_light(f32x4 (&acc)[8][4], LAS unsigned char* lds, const GemmT& T, ...
;     ...
;     G_ISSUE_B(0); G_DMA_A(0, 0, 0); G_DMA_A(0, 0, 1); G_DMA_A(0, 0, 2); G_DMA_A(0, 0, 3); G_RETIRE(); G_WRITE_B(0);
;     if (nt > 1) G_ISSUE_B(1);
;     G_BAR();
;     ...
;         if (w1) { G_RETIRE(); G_WRITE_B(cur ^ 1); }
;         if (i2) G_ISSUE_B(t + 2);
.Lmy_rcgP0:
	s_cmp_lt_i32 s99, 65
	s_cbranch_scc1 .Lmy_rcgP1
	buffer_load_dwordx4 v[240:243], v222, s[36:39], s101 offen
.Lmy_rcgP1:
	buffer_load_dwordx4 v[162:165], v225, s[24:27], s67 offen
	buffer_load_dwordx4 v[166:169], v225, s[24:27], s76 offen
	buffer_load_dwordx4 v[170:173], v225, s[24:27], s77 offen
	buffer_load_dwordx4 v[174:177], v225, s[24:27], s78 offen
	buffer_load_dwordx4 v[178:181], v225, s[24:27], s79 offen
	buffer_load_dwordx4 v[182:185], v225, s[24:27], s80 offen
	buffer_load_dwordx4 v[186:189], v225, s[24:27], s81 offen
	buffer_load_dwordx4 v[190:193], v225, s[24:27], s82 offen
	s_cmp_gt_i32 s1, 0
	s_cselect_b64 s[62:63], -1, 0
	s_cmp_lg_u32 s1, 1
	v_cvt_pk_bf16_f32 v36, v12, v32
	v_cvt_pk_bf16_f32 v37, v20, v4
	v_cvt_pk_bf16_f32 v38, v24, v8
	v_cvt_pk_bf16_f32 v39, v28, v16
	s_cselect_b64 s[60:61], -1, 0
	s_cmp_gt_i32 s1, 2
	ds_write_b128 v228, v[36:39] offset:32768
	v_cvt_pk_bf16_f32 v36, v13, v33
	v_cvt_pk_bf16_f32 v37, v21, v5
	v_cvt_pk_bf16_f32 v38, v25, v9
	v_cvt_pk_bf16_f32 v39, v29, v17
	s_cselect_b64 s[58:59], -1, 0
	s_cmp_gt_i32 s1, 3
	ds_write_b128 v228, v[36:39] offset:32832
	v_cvt_pk_bf16_f32 v36, v14, v34
	v_cvt_pk_bf16_f32 v37, v22, v6
	v_cvt_pk_bf16_f32 v38, v26, v10
	v_cvt_pk_bf16_f32 v39, v30, v18
	v_cvt_pk_bf16_f32 v4, v15, v35
	v_cvt_pk_bf16_f32 v5, v23, v7
	v_cvt_pk_bf16_f32 v6, v27, v11
	v_cvt_pk_bf16_f32 v7, v31, v19
	v_add_u32_e32 v3, v227, v218
	s_cselect_b64 s[54:55], -1, 0
	s_cmp_gt_i32 s1, 4
	ds_write_b128 v228, v[36:39] offset:32896
	ds_write_b128 v3, v[4:7] offset:32768
	s_cselect_b64 s[46:47], -1, 0
	s_cmp_gt_i32 s1, 5
	s_waitcnt lgkmcnt(0)
	s_barrier
	s_cselect_b64 s[44:45], -1, 0
	s_cmp_gt_i32 s1, 6
	v_mov_b32_e32 v4, v2
	v_mov_b32_e32 v5, v2
	s_cselect_b64 s[34:35], -1, 0
	s_cmp_gt_i32 s1, 7
	v_mov_b32_e32 v3, v2
	v_mov_b64_e32 v[16:17], v[4:5]
	v_mov_b64_e32 v[8:9], v[4:5]
	v_mov_b64_e32 v[20:21], v[4:5]
	v_mov_b64_e32 v[12:13], v[4:5]
	v_mov_b64_e32 v[32:33], v[4:5]
	v_mov_b64_e32 v[24:25], v[4:5]
	v_mov_b64_e32 v[36:37], v[4:5]
	v_mov_b64_e32 v[28:29], v[4:5]
	v_mov_b64_e32 v[48:49], v[4:5]
	v_mov_b64_e32 v[40:41], v[4:5]
	v_mov_b64_e32 v[52:53], v[4:5]
	v_mov_b64_e32 v[44:45], v[4:5]
	v_mov_b64_e32 v[64:65], v[4:5]
	v_mov_b64_e32 v[56:57], v[4:5]
	v_mov_b64_e32 v[68:69], v[4:5]
	v_mov_b64_e32 v[60:61], v[4:5]
	v_mov_b64_e32 v[80:81], v[4:5]
	v_mov_b64_e32 v[72:73], v[4:5]
	v_mov_b64_e32 v[84:85], v[4:5]
	v_mov_b64_e32 v[76:77], v[4:5]
	v_mov_b64_e32 v[96:97], v[4:5]
	v_mov_b64_e32 v[88:89], v[4:5]
	v_mov_b64_e32 v[100:101], v[4:5]
	v_mov_b64_e32 v[92:93], v[4:5]
	v_mov_b64_e32 v[112:113], v[4:5]
	v_mov_b64_e32 v[104:105], v[4:5]
	v_mov_b64_e32 v[140:141], v[4:5]
	v_mov_b64_e32 v[108:109], v[4:5]
	v_mov_b64_e32 v[160:161], v[4:5]
	v_mov_b64_e32 v[152:153], v[4:5]
	v_mov_b64_e32 v[196:197], v[4:5]
	v_mov_b64_e32 v[156:157], v[4:5]
	s_mov_b32 s68, 0
	s_cselect_b64 s[22:23], -1, 0
	s_mov_b32 s69, 0x10e000
	s_movk_i32 s70, 0x80
	v_mov_b64_e32 v[14:15], v[2:3]
	v_mov_b64_e32 v[6:7], v[2:3]
	v_mov_b64_e32 v[18:19], v[2:3]
	v_mov_b64_e32 v[10:11], v[2:3]
	v_mov_b64_e32 v[30:31], v[2:3]
	v_mov_b64_e32 v[22:23], v[2:3]
	v_mov_b64_e32 v[34:35], v[2:3]
	v_mov_b64_e32 v[26:27], v[2:3]
	v_mov_b64_e32 v[46:47], v[2:3]
	v_mov_b64_e32 v[38:39], v[2:3]
	v_mov_b64_e32 v[50:51], v[2:3]
	v_mov_b64_e32 v[42:43], v[2:3]
	v_mov_b64_e32 v[62:63], v[2:3]
	v_mov_b64_e32 v[54:55], v[2:3]
	v_mov_b64_e32 v[66:67], v[2:3]
	v_mov_b64_e32 v[58:59], v[2:3]
	v_mov_b64_e32 v[78:79], v[2:3]
	v_mov_b64_e32 v[70:71], v[2:3]
	v_mov_b64_e32 v[82:83], v[2:3]
	v_mov_b64_e32 v[74:75], v[2:3]
	v_mov_b64_e32 v[94:95], v[2:3]
	v_mov_b64_e32 v[86:87], v[2:3]
	v_mov_b64_e32 v[98:99], v[2:3]
	v_mov_b64_e32 v[90:91], v[2:3]
	v_mov_b64_e32 v[110:111], v[2:3]
	v_mov_b64_e32 v[102:103], v[2:3]
	v_mov_b64_e32 v[138:139], v[2:3]
	v_mov_b64_e32 v[106:107], v[2:3]
	v_mov_b64_e32 v[158:159], v[2:3]
	v_mov_b64_e32 v[150:151], v[2:3]
	v_mov_b64_e32 v[194:195], v[2:3]
	v_mov_b64_e32 v[154:155], v[2:3]
	s_cmp_ge_i32 s100, 32
	s_cbranch_scc0 .Lmy_d2g_nopre
	s_mov_b32 s98, 0x10e000
	s_add_i32 s6, s98, 0xffff2000
	buffer_load_dwordx4 v[8:11], v225, s[24:27], s6 offen
	s_add_i32 s7, s98, 0xffff4000
	buffer_load_dwordx4 v[12:15], v225, s[24:27], s7 offen
	s_add_i32 s6, s98, 0xffff6000
	buffer_load_dwordx4 v[16:19], v225, s[24:27], s6 offen
	s_add_i32 s7, s98, 0xffff8000
	buffer_load_dwordx4 v[20:23], v225, s[24:27], s7 offen
	s_add_i32 s6, s98, 0xffffa000
	buffer_load_dwordx4 v[24:27], v225, s[24:27], s6 offen
	s_add_i32 s7, s98, 0xffffc000
	buffer_load_dwordx4 v[28:31], v225, s[24:27], s7 offen
	s_add_i32 s6, s98, 0xffffe000
	buffer_load_dwordx4 v[32:35], v225, s[24:27], s6 offen
	buffer_load_dwordx4 v[36:39], v225, s[24:27], s98 offen
.Lmy_d2g_nopre:
	s_branch .LBB0_1175
.LBB0_1174:
	s_cmp_ge_i32 s100, 32
	s_cbranch_scc1 .Lmy_d2g_s47
	s_waitcnt vmcnt(0)
	v_add_u32_e32 v244, s71, v229
	s_add_i32 s101, s70, 0x80
	s_cmp_le_i32 s99, s100
	s_cbranch_scc1 .Lmy_rcgL0
	ds_write_b128 v244, v[236:239]
	buffer_load_dwordx4 v[236:239], v223, s[36:39], s101 offen
.Lmy_rcgL0:
	s_cmp_lt_i32 s99, 65
	s_cbranch_scc1 .Lmy_rcgL1
	ds_write_b128 v244, v[240:243] offset:8192
	buffer_load_dwordx4 v[240:243], v222, s[36:39], s101 offen
.Lmy_rcgL1:
	s_add_i32 s6, s69, 0xffff2000
	v_cvt_pk_bf16_f32 v198, v162, v166
	v_cvt_pk_bf16_f32 v202, v163, v167
	v_cvt_pk_bf16_f32 v206, v164, v168
	v_cvt_pk_bf16_f32 v210, v165, v169
	s_add_i32 s7, s69, 0xffff4000
	buffer_load_dwordx4 v[162:165], v225, s[24:27], s6 offen
	buffer_load_dwordx4 v[166:169], v225, s[24:27], s7 offen
	s_add_i32 s6, s69, 0xffff6000
	v_cvt_pk_bf16_f32 v199, v170, v174
	v_cvt_pk_bf16_f32 v203, v171, v175
	v_cvt_pk_bf16_f32 v207, v172, v176
	v_cvt_pk_bf16_f32 v211, v173, v177
	s_add_i32 s7, s69, 0xffff8000
	buffer_load_dwordx4 v[170:173], v225, s[24:27], s6 offen
	buffer_load_dwordx4 v[174:177], v225, s[24:27], s7 offen
	s_add_i32 s6, s69, 0xffffa000
	v_cvt_pk_bf16_f32 v200, v178, v182
	v_cvt_pk_bf16_f32 v204, v179, v183
	v_cvt_pk_bf16_f32 v208, v180, v184
	v_cvt_pk_bf16_f32 v212, v181, v185
	s_add_i32 s7, s69, 0xffffc000
	buffer_load_dwordx4 v[178:181], v225, s[24:27], s6 offen
	buffer_load_dwordx4 v[182:185], v225, s[24:27], s7 offen
	s_add_i32 s6, s69, 0xffffe000
	v_cvt_pk_bf16_f32 v201, v186, v190
	v_cvt_pk_bf16_f32 v205, v187, v191
	v_cvt_pk_bf16_f32 v209, v188, v192
	v_cvt_pk_bf16_f32 v213, v189, v193
	buffer_load_dwordx4 v[186:189], v225, s[24:27], s6 offen
	buffer_load_dwordx4 v[190:193], v225, s[24:27], s69 offen
	s_branch .Lmy_d2g_wr
.Lmy_d2g_s47:
	s_waitcnt vmcnt(8)
	v_add_u32_e32 v244, s71, v229
	s_add_i32 s101, s70, 0x80
	s_cmp_le_i32 s99, s100
	s_cbranch_scc1 .Lmy_rcgM0
	ds_write_b128 v244, v[236:239]
	buffer_load_dwordx4 v[236:239], v223, s[36:39], s101 offen

; #define LAS __attribute__((address_space(3)))
; #define G_DMA_A(buf, t, i_) __builtin_amdgcn_raw_ptr_buffer_load_lds(ra, (LAS void*)(lds + (buf) * 65536 + a_wu + (i_) * 8192), 16, ao##i_, (unsigned)(t) * 128u, 0, 0)
; #define G_ISSUE_B(t) do { const unsigned so_ = (unsigned)(t) * 64u * ldbB; _Pragma("unroll") for (int i_ = 0; i_ < 8; ++i_) sb[i_] = __builtin_bit_cast(f32x4, __builtin_amdgcn_raw_buffer_load_b128(rb, bo, so_ + (unsigned)i_ * ldbB, 0)); } while (0)
; #define G_RETIRE() asm volatile("s_waitcnt vmcnt(0)" : "+v"(sb[0]), "+v"(sb[1]), "+v"(sb[2]), "+v"(sb[3]), "+v"(sb[4]), "+v"(sb[5]), "+v"(sb[6]), "+v"(sb[7]) :: "memory")
; #define G_WRITE_B(buf) do { LAS unsigned char* d_ = lds + (buf) * 65536; \
;         _Pragma("unroll") for (int j_ = 0; j_ < 4; ++j_) { u32x4 w_; w_.x = cvtpk(sb[0][j_], sb[1][j_]); w_.y = cvtpk(sb[2][j_], sb[3][j_]); w_.z = cvtpk(sb[4][j_], sb[5][j_]); w_.w = cvtpk(sb[6][j_], sb[7][j_]); \
;             *(LAS u32x4*)(d_ + 32768 + T.b_w + ((T.b_rot + 64u * j_) & 255u)) = w_; } } while (0)
; #define G_DMA_A(buf, t, i_) __builtin_amdgcn_raw_ptr_buffer_load_lds(ra, (LAS void*)(lds + (buf) * 65536 + a_wu + (i_) * 8192), 16, ao##i_, (unsigned)(t) * 128u, 0, 0)
; __device__ __forceinline__ void gemm_kloop_light(f32x4 (&acc)[8][4], LAS unsigned char* lds, const GemmT& T, ...
;     ...
;     for (int t = 0; t < nt; ++t) { const int cur = t & 1; const bool w1 = t + 1 < nt, i2 = t + 2 < nt;
;         if (w1) { G_DMA_A(cur ^ 1, t + 1, 0); G_DMA_A(cur ^ 1, t + 1, 1); G_DMA_A(cur ^ 1, t + 1, 2); G_DMA_A(cur ^ 1, t + 1, 3); }
;         if (mlim > 0) {
; #pragma unroll
;             for (int ks = 0; ks < 2; ++ks) { const LAS unsigned char* s_ = lds + cur * 65536 + ks * 1024; bf16x8 Bf_[4];
; #pragma unroll
;                 for (int n_ = 0; n_ < 4; ++n_) Bf_[n_] = *(const LAS bf16x8*)(s_ + T.b_r + n_ * 2048);
; #pragma unroll
;                 for (int m_ = 0; m_ < 8; ++m_) if (m_ < mlim) { const bf16x8 At_ = *(const LAS bf16x8*)(s_ + T.a_r + m_ * 2048);
; #pragma unroll
;                     for (int n_ = 0; n_ < 4; ++n_) acc[m_][n_] = __builtin_amdgcn_mfma_f32_16x16x32_bf16(Bf_[n_], At_, acc[m_][n_], 0, 0, 0); } } }
;         if (w1) { G_RETIRE(); G_WRITE_B(cur ^ 1); }
;         if (i2) G_ISSUE_B(t + 2);
.Lmy_rcgM1:
	s_bitcmp1_b32 s68, 16
	s_cbranch_scc1 .Lmy_d2g_odd
	v_cvt_pk_bf16_f32 v198, v162, v166
	v_cvt_pk_bf16_f32 v199, v170, v174
	v_cvt_pk_bf16_f32 v200, v178, v182
	v_cvt_pk_bf16_f32 v201, v186, v190
	v_cvt_pk_bf16_f32 v202, v163, v167
	v_cvt_pk_bf16_f32 v203, v171, v175
	v_cvt_pk_bf16_f32 v204, v179, v183
	v_cvt_pk_bf16_f32 v205, v187, v191
	v_cvt_pk_bf16_f32 v206, v164, v168
	v_cvt_pk_bf16_f32 v207, v172, v176
	v_cvt_pk_bf16_f32 v208, v180, v184
	v_cvt_pk_bf16_f32 v209, v188, v192
	v_cvt_pk_bf16_f32 v210, v165, v169
	v_cvt_pk_bf16_f32 v211, v173, v177
	v_cvt_pk_bf16_f32 v212, v181, v185
	v_cvt_pk_bf16_f32 v213, v189, v193
	s_cmp_gt_u32 s69, 0xf0e000
	s_cbranch_scc1 .Lmy_d2g_wr
	s_add_i32 s6, s69, 0x72000
	buffer_load_dwordx4 v[162:165], v225, s[24:27], s6 offen
	s_add_i32 s7, s69, 0x74000
	buffer_load_dwordx4 v[166:169], v225, s[24:27], s7 offen
	s_add_i32 s6, s69, 0x76000
	buffer_load_dwordx4 v[170:173], v225, s[24:27], s6 offen
	s_add_i32 s7, s69, 0x78000
	buffer_load_dwordx4 v[174:177], v225, s[24:27], s7 offen
	s_add_i32 s6, s69, 0x7a000
	buffer_load_dwordx4 v[178:181], v225, s[24:27], s6 offen
	s_add_i32 s7, s69, 0x7c000
	buffer_load_dwordx4 v[182:185], v225, s[24:27], s7 offen
	s_add_i32 s6, s69, 0x7e000
	buffer_load_dwordx4 v[186:189], v225, s[24:27], s6 offen
	s_add_i32 s7, s69, 0x80000
	buffer_load_dwordx4 v[190:193], v225, s[24:27], s7 offen
	s_branch .Lmy_d2g_wr
.Lmy_d2g_odd:
	v_cvt_pk_bf16_f32 v198, v8, v12
	v_cvt_pk_bf16_f32 v199, v16, v20
	v_cvt_pk_bf16_f32 v200, v24, v28
	v_cvt_pk_bf16_f32 v201, v32, v36
	v_cvt_pk_bf16_f32 v202, v9, v13
	v_cvt_pk_bf16_f32 v203, v17, v21
	v_cvt_pk_bf16_f32 v204, v25, v29
	v_cvt_pk_bf16_f32 v205, v33, v37
	v_cvt_pk_bf16_f32 v206, v10, v14
	v_cvt_pk_bf16_f32 v207, v18, v22
	v_cvt_pk_bf16_f32 v208, v26, v30
	v_cvt_pk_bf16_f32 v209, v34, v38
	v_cvt_pk_bf16_f32 v210, v11, v15
	v_cvt_pk_bf16_f32 v211, v19, v23
	v_cvt_pk_bf16_f32 v212, v27, v31
	v_cvt_pk_bf16_f32 v213, v35, v39
	s_cmp_gt_u32 s69, 0xf0e000
	s_cbranch_scc1 .Lmy_d2g_wr
	s_add_i32 s6, s69, 0x72000
	buffer_load_dwordx4 v[8:11], v225, s[24:27], s6 offen
	s_add_i32 s7, s69, 0x74000
	buffer_load_dwordx4 v[12:15], v225, s[24:27], s7 offen
	s_add_i32 s6, s69, 0x76000
	buffer_load_dwordx4 v[16:19], v225, s[24:27], s6 offen
	s_add_i32 s7, s69, 0x78000
	buffer_load_dwordx4 v[20:23], v225, s[24:27], s7 offen
	s_add_i32 s6, s69, 0x7a000
	buffer_load_dwordx4 v[24:27], v225, s[24:27], s6 offen
	s_add_i32 s7, s69, 0x7c000
	buffer_load_dwordx4 v[28:31], v225, s[24:27], s7 offen
	s_add_i32 s6, s69, 0x7e000
	buffer_load_dwordx4 v[32:35], v225, s[24:27], s6 offen
	s_add_i32 s7, s69, 0x80000
	buffer_load_dwordx4 v[36:39], v225, s[24:27], s7 offen
.Lmy_d2g_wr:
	v_add_u32_e32 v3, s71, v227
	v_add_u32_e32 v4, v3, v220
	v_add_u32_e32 v3, v3, v218
	ds_write_b128 v4, v[198:201] offset:32768
	ds_write_b128 v4, v[202:205] offset:32832
	ds_write_b128 v4, v[206:209] offset:32896
	ds_write_b128 v3, v[210:213] offset:32768
	s_waitcnt lgkmcnt(0)
	s_barrier
	s_add_i32 s69, s69, 0x80000
	s_add_i32 s68, s68, 0x10000
	s_addk_i32 s70, 0x80
	s_cmp_eq_u32 s69, 0x100e000
	s_cbranch_scc1 .LBB0_1204
.LBB0_1175:
	s_and_b32 s6, s68, 0x10000
	s_xor_b32 s71, s6, 0x10000
	v_cndmask_b32_e64 v3, 0, 1, s[62:63]
	s_andn2_b64 vcc, exec, s[62:63]
	v_cmp_ne_u32_e64 s[4:5], 1, v3
	s_cbranch_vccnz .LBB0_1174
	s_add_i32 s6, s6, 0
	v_add_u32_e32 v4, s6, v226
	ds_read_b128 v[198:201], v4 offset:32768
	v_add_u32_e32 v3, s6, v216
	ds_read_b128 v[202:205], v4 offset:34816
	ds_read_b128 v[230:233], v3
	ds_read_b128 v[206:209], v4 offset:36864
	ds_read_b128 v[210:213], v4 offset:38912
	s_waitcnt lgkmcnt(2)
	v_mfma_f32_16x16x32_bf16 v[194:197], v[202:205], v[230:233], v[194:197]
	v_cndmask_b32_e64 v5, 0, 1, s[60:61]
	v_cmp_ne_u32_e64 s[6:7], 1, v5
	s_andn2_b64 vcc, exec, s[60:61]
	v_mfma_f32_16x16x32_bf16 v[154:157], v[198:201], v[230:233], v[154:157]
	s_waitcnt lgkmcnt(1)
	v_mfma_f32_16x16x32_bf16 v[150:153], v[206:209], v[230:233], v[150:153]
	s_waitcnt lgkmcnt(0)
	v_mfma_f32_16x16x32_bf16 v[158:161], v[210:213], v[230:233], v[158:161]
	s_cbranch_vccnz .LBB0_1191
	ds_read_b128 v[230:233], v3 offset:2048
	s_waitcnt lgkmcnt(0)
	v_mfma_f32_16x16x32_bf16 v[106:109], v[198:201], v[230:233], v[106:109]
	v_mfma_f32_16x16x32_bf16 v[138:141], v[202:205], v[230:233], v[138:141]
	v_mfma_f32_16x16x32_bf16 v[102:105], v[206:209], v[230:233], v[102:105]
	v_mfma_f32_16x16x32_bf16 v[110:113], v[210:213], v[230:233], v[110:113]
	v_cndmask_b32_e64 v5, 0, 1, s[58:59]
	v_cmp_ne_u32_e64 s[8:9], 1, v5
	s_andn2_b64 vcc, exec, s[58:59]
	s_cbranch_vccz .LBB0_1192

; #define LAS __attribute__((address_space(3)))
; #define G_DMA_A(buf, t, i_) __builtin_amdgcn_raw_ptr_buffer_load_lds(ra, (LAS void*)(lds + (buf) * 65536 + a_wu + (i_) * 8192), 16, ao##i_, (unsigned)(t) * 128u, 0, 0)
; #define G_DMA_A(buf, t, i_) __builtin_amdgcn_raw_ptr_buffer_load_lds(ra, (LAS void*)(lds + (buf) * 65536 + a_wu + (i_) * 8192), 16, ao##i_, (unsigned)(t) * 128u, 0, 0)
; __device__ __forceinline__ void gemm_kloop_light(f32x4 (&acc)[8][4], LAS unsigned char* lds, const GemmT& T, ...
;     ...
;     for (int t = 0; t < nt; ++t) { const int cur = t & 1; const bool w1 = t + 1 < nt, i2 = t + 2 < nt;
;         if (w1) { G_DMA_A(cur ^ 1, t + 1, 0); G_DMA_A(cur ^ 1, t + 1, 1); G_DMA_A(cur ^ 1, t + 1, 2); G_DMA_A(cur ^ 1, t + 1, 3); }
;         if (mlim > 0) {
; #pragma unroll
;             for (int ks = 0; ks < 2; ++ks) { const LAS unsigned char* s_ = lds + cur * 65536 + ks * 1024; bf16x8 Bf_[4];
; #pragma unroll
;                 for (int n_ = 0; n_ < 4; ++n_) Bf_[n_] = *(const LAS bf16x8*)(s_ + T.b_r + n_ * 2048);
; #pragma unroll
;                 for (int m_ = 0; m_ < 8; ++m_) if (m_ < mlim) { const bf16x8 At_ = *(const LAS bf16x8*)(s_ + T.a_r + m_ * 2048);
; #pragma unroll
;                     for (int n_ = 0; n_ < 4; ++n_) acc[m_][n_] = __builtin_amdgcn_mfma_f32_16x16x32_bf16(Bf_[n_], At_, acc[m_][n_], 0, 0, 0); } } }
.LBB0_1204:
	s_add_i32 s6, s3, 0x16000
	s_add_i32 s7, s3, 0x14000
	s_add_i32 s3, s3, 0x12000
	s_mov_b32 s38, s26
	s_mov_b32 s39, s27
	v_cndmask_b32_e64 v3, 0, 1, s[60:61]
	s_and_b64 vcc, exec, s[4:5]
	v_cmp_ne_u32_e64 s[6:7], 1, v3
	s_cbranch_vccnz .LBB0_1221
	v_add_u32_e32 v4, 0, v226
	ds_read_b128 v[198:201], v4 offset:32768
	v_add_u32_e32 v3, 0, v216
	ds_read_b128 v[202:205], v4 offset:34816
	ds_read_b128 v[230:233], v3
	ds_read_b128 v[206:209], v4 offset:36864
	ds_read_b128 v[210:213], v4 offset:38912
	s_waitcnt lgkmcnt(2)
	v_mfma_f32_16x16x32_bf16 v[194:197], v[202:205], v[230:233], v[194:197]
	s_and_b64 vcc, exec, s[6:7]
	v_mfma_f32_16x16x32_bf16 v[154:157], v[198:201], v[230:233], v[154:157]
	s_waitcnt lgkmcnt(1)
	v_mfma_f32_16x16x32_bf16 v[150:153], v[206:209], v[230:233], v[150:153]
	s_waitcnt lgkmcnt(0)
	v_mfma_f32_16x16x32_bf16 v[158:161], v[210:213], v[230:233], v[158:161]
	s_cbranch_vccnz .LBB0_1239
	ds_read_b128 v[230:233], v3 offset:2048
	s_waitcnt lgkmcnt(0)
	v_mfma_f32_16x16x32_bf16 v[106:109], v[198:201], v[230:233], v[106:109]
	v_mfma_f32_16x16x32_bf16 v[138:141], v[202:205], v[230:233], v[138:141]
	v_mfma_f32_16x16x32_bf16 v[102:105], v[206:209], v[230:233], v[102:105]
	v_mfma_f32_16x16x32_bf16 v[110:113], v[210:213], v[230:233], v[110:113]
	v_cndmask_b32_e64 v5, 0, 1, s[58:59]
	v_cmp_ne_u32_e64 s[8:9], 1, v5
	s_andn2_b64 vcc, exec, s[58:59]
	s_cbranch_vccz .LBB0_1240

; #define G_ISSUE_B(t) do { const unsigned so_ = (unsigned)(t) * 64u * ldbB; _Pragma("unroll") for (int i_ = 0; i_ < 8; ++i_) sb[i_] = __builtin_bit_cast(f32x4, __builtin_amdgcn_raw_buffer_load_b128(rb, bo, so_ + (unsigned)i_ * ldbB, 0)); } while (0)
; #define G_RETIRE() asm volatile("s_waitcnt vmcnt(0)" : "+v"(sb[0]), "+v"(sb[1]), "+v"(sb[2]), "+v"(sb[3]), "+v"(sb[4]), "+v"(sb[5]), "+v"(sb[6]), "+v"(sb[7]) :: "memory")
; #define G_WRITE_B(buf) do { LAS unsigned char* d_ = lds + (buf) * 65536; \
;         _Pragma("unroll") for (int j_ = 0; j_ < 4; ++j_) { u32x4 w_; w_.x = cvtpk(sb[0][j_], sb[1][j_]); w_.y = cvtpk(sb[2][j_], sb[3][j_]); w_.z = cvtpk(sb[4][j_], sb[5][j_]); w_.w = cvtpk(sb[6][j_], sb[7][j_]); \
;             *(LAS u32x4*)(d_ + 32768 + T.b_w + ((T.b_rot + 64u * j_) & 255u)) = w_; } } while (0)
; #define G_BAR() do { asm volatile("s_waitcnt lgkmcnt(0)" ::: "memory"); __builtin_amdgcn_s_barrier(); asm volatile("" ::: "memory"); } while (0)
; #define G_ISSUE_B(t) do { const unsigned so_ = (unsigned)(t) * 64u * ldbB; _Pragma("unroll") for (int i_ = 0; i_ < 8; ++i_) sb[i_] = __builtin_bit_cast(f32x4, __builtin_amdgcn_raw_buffer_load_b128(rb, bo, so_ + (unsigned)i_ * ldbB, 0)); } while (0)
; #define G_RETIRE() asm volatile("s_waitcnt vmcnt(0)" : "+v"(sb[0]), "+v"(sb[1]), "+v"(sb[2]), "+v"(sb[3]), "+v"(sb[4]), "+v"(sb[5]), "+v"(sb[6]), "+v"(sb[7]) :: "memory")
; #define G_WRITE_B(buf) do { LAS unsigned char* d_ = lds + (buf) * 65536; \
;         _Pragma("unroll") for (int j_ = 0; j_ < 4; ++j_) { u32x4 w_; w_.x = cvtpk(sb[0][j_], sb[1][j_]); w_.y = cvtpk(sb[2][j_], sb[3][j_]); w_.z = cvtpk(sb[4][j_], sb[5][j_]); w_.w = cvtpk(sb[6][j_], sb[7][j_]); \
;             *(LAS u32x4*)(d_ + 32768 + T.b_w + ((T.b_rot + 64u * j_) & 255u)) = w_; } } while (0)
; __device__ __forceinline__ void gemm_kloop_light(f32x4 (&acc)[8][4], LAS unsigned char* lds, const GemmT& T, ...
;     ...
;         if (w1) { G_RETIRE(); G_WRITE_B(cur ^ 1); }
;         if (i2) G_ISSUE_B(t + 2);
;         G_BAR(); }
.LBB0_1221:
	v_add_u32_e32 v3, s29, v219
	s_waitcnt vmcnt(4)
	s_waitcnt vmcnt(0)
	v_add_u32_e32 v244, 0x10000, v229
	s_cmp_le_i32 s99, s100
	s_cbranch_scc1 .Lmy_rcgT0
	ds_write_b128 v244, v[236:239]
.Lmy_rcgT0:
	s_cmp_lt_i32 s99, 65
	s_cbranch_scc1 .Lmy_rcgT1
	ds_write_b128 v244, v[240:243] offset:8192
.Lmy_rcgT1:
	v_add_u32_e32 v4, v3, v220
	v_cvt_pk_bf16_f32 v198, v162, v166
	v_cvt_pk_bf16_f32 v199, v170, v174
	v_cvt_pk_bf16_f32 v200, v178, v182
	v_cvt_pk_bf16_f32 v201, v186, v190
	ds_write_b128 v4, v[198:201]
	v_cvt_pk_bf16_f32 v198, v163, v167
	v_cvt_pk_bf16_f32 v199, v171, v175
	v_cvt_pk_bf16_f32 v200, v179, v183
	v_cvt_pk_bf16_f32 v201, v187, v191
	ds_write_b128 v4, v[198:201] offset:64
	v_cvt_pk_bf16_f32 v198, v164, v168
	v_cvt_pk_bf16_f32 v199, v172, v176
	v_cvt_pk_bf16_f32 v200, v180, v184
	v_cvt_pk_bf16_f32 v201, v188, v192
	v_cvt_pk_bf16_f32 v162, v165, v169
	v_cvt_pk_bf16_f32 v163, v173, v177
	v_cvt_pk_bf16_f32 v164, v181, v185
	v_cvt_pk_bf16_f32 v165, v189, v193
	v_add_u32_e32 v3, v3, v218
	ds_write_b128 v4, v[198:201] offset:128
	ds_write_b128 v3, v[162:165]
	s_waitcnt lgkmcnt(0)
	s_barrier
	s_and_b64 vcc, exec, s[4:5]
	s_cbranch_vccnz .LBB0_1238
	s_add_i32 s3, 0, 0x10000
	v_add_u32_e32 v4, s3, v217
	ds_read_b128 v[166:169], v4
	v_add_u32_e32 v3, s3, v216
	ds_read_b128 v[170:173], v4 offset:2048
	ds_read_b128 v[182:185], v3
	ds_read_b128 v[174:177], v4 offset:4096
	ds_read_b128 v[178:181], v4 offset:6144
	s_waitcnt lgkmcnt(2)
	v_mfma_f32_16x16x32_bf16 v[162:165], v[170:173], v[182:185], v[194:197]
	s_and_b64 vcc, exec, s[6:7]
	v_mfma_f32_16x16x32_bf16 v[154:157], v[166:169], v[182:185], v[154:157]
	s_waitcnt lgkmcnt(1)
	v_mfma_f32_16x16x32_bf16 v[150:153], v[174:177], v[182:185], v[150:153]
	s_waitcnt lgkmcnt(0)
	v_mfma_f32_16x16x32_bf16 v[158:161], v[178:181], v[182:185], v[158:161]
	s_cbranch_vccnz .LBB0_1251
	ds_read_b128 v[182:185], v3 offset:2048
	s_waitcnt lgkmcnt(0)
	v_mfma_f32_16x16x32_bf16 v[106:109], v[166:169], v[182:185], v[106:109]
	v_mfma_f32_16x16x32_bf16 v[138:141], v[170:173], v[182:185], v[138:141]
	v_mfma_f32_16x16x32_bf16 v[102:105], v[174:177], v[182:185], v[102:105]
	v_mfma_f32_16x16x32_bf16 v[110:113], v[178:181], v[182:185], v[110:113]
	s_cmp_gt_u32 s1, 2
	s_cselect_b64 s[4:5], -1, 0
	s_cmp_lt_u32 s1, 3
	s_cbranch_scc0 .LBB0_1252

; __device__ __forceinline__ int tid_opaque() { int t = threadIdx.x; asm volatile("" : "+v"(t)); return t; }
; #define G_DMA_A(buf, t, i_) __builtin_amdgcn_raw_ptr_buffer_load_lds(ra, (LAS void*)(lds + (buf) * 65536 + a_wu + (i_) * 8192), 16, ao##i_, (unsigned)(t) * 128u, 0, 0)
; #define G_ISSUE_B(t) do { const unsigned so_ = (unsigned)(t) * 64u * ldbB; _Pragma("unroll") for (int i_ = 0; i_ < 8; ++i_) sb[i_] = __builtin_bit_cast(f32x4, __builtin_amdgcn_raw_buffer_load_b128(rb, bo, so_ + (unsigned)i_ * ldbB, 0)); } while (0)
; #define G_RETIRE() asm volatile("s_waitcnt vmcnt(0)" : "+v"(sb[0]), "+v"(sb[1]), "+v"(sb[2]), "+v"(sb[3]), "+v"(sb[4]), "+v"(sb[5]), "+v"(sb[6]), "+v"(sb[7]) :: "memory")
; #define G_BAR() do { asm volatile("s_waitcnt lgkmcnt(0)" ::: "memory"); __builtin_amdgcn_s_barrier(); asm volatile("" ::: "memory"); } while (0)
; __device__ __forceinline__ void gemm_kloop_light(f32x4 (&acc)[8][4], LAS unsigned char* lds, const GemmT& T, ...
;     ...
;     G_ISSUE_B(0); G_DMA_A(0, 0, 0); G_DMA_A(0, 0, 1); G_DMA_A(0, 0, 2); G_DMA_A(0, 0, 3); G_RETIRE(); G_WRITE_B(0);
;     if (nt > 1) G_ISSUE_B(1);
;     G_BAR();
; __device__ __forceinline__ void phase_moe_down(const Ptrs& p, LAS unsigned char* lds) {
;     ...
;         GemmT T; T.init();
;         const int* list = (const int*)(p.ws + OFF_LIST) + (size_t)mu.e * NTOK; const int i0 = mu.mt * 256, col0 = mu.nt * 256;
;         const unsigned ao = (unsigned)((T.aR * D + T.aC) * 2), bo = (unsigned)((T.b_k * D + T.b_col) * 4);
;         int pa = -1; float pg = 0.f;
;         { const int t_ = tid_opaque(); if (t_ < 256 && i0 + t_ < mu.cnt) { pa = list[i0 + t_]; pg = gate[pa]; } }
;         f32x4 acc[8][4]; acc_zero(acc);
;         const int mlim = __builtin_amdgcn_readfirstlane(T.wr) ? 0 : ((mu.cnt - i0 + 15) >> 4);
;         if (mu.light) gemm_kloop_light(acc, lds, T, mk_rsrc(act + (size_t)(mu.base + i0) * D), ao, ao + 64u * 4096, ao + 128u * 4096, ao + 192u * 4096,
;                                        mk_rsrc(p.w_down + (size_t)mu.e * D * D + col0), bo, D * 4u, D / 64, mlim);
;         else gemm_kloop(acc, lds, T, mk_rsrc(act + (size_t)(mu.base + i0) * D), ao, ao + 64u * 4096, ao + 128u * 4096, ao + 192u * 4096,
;                         mk_rsrc(p.w_down + (size_t)mu.e * D * D + col0), bo, D * 4u, D / 64);
.LBB0_1483:
	s_or_b64 exec, exec, s[0:1]
	s_add_i32 s2, s84, s85
	s_ashr_i32 s3, s2, 31
	s_lshl_b32 s0, s81, 8
	s_lshl_b64 s[2:3], s[2:3], 12
	s_add_u32 s36, s20, s2
	v_readlane_b32 s4, v246, 0
	s_addc_u32 s1, s28, s3
	v_readlane_b32 s5, v246, 1
	v_readlane_b32 s6, v246, 2
	v_readlane_b32 s7, v246, 3
	v_readlane_b32 s8, v246, 4
	v_readlane_b32 s9, v246, 5
	s_and_b32 s37, s1, 0xffff
	s_lshl_b64 s[2:3], s[42:43], 24
	v_readlane_b32 s10, v246, 6
	v_readlane_b32 s11, v246, 7
	s_mov_b64 s[4:5], s[8:9]
	s_add_u32 s4, s4, s2
	v_ashrrev_i32_e32 v4, 6, v3
	v_bfe_u32 v11, v3, 1, 2
	s_addc_u32 s5, s5, s3
	s_ashr_i32 s1, s0, 31
	v_ashrrev_i32_e32 v5, 7, v3
	v_and_b32_e32 v6, 1, v4
	v_bfe_u32 v8, v3, 5, 1
	v_bfe_u32 v10, v3, 3, 2
	v_and_b32_e32 v12, 1, v3
	v_lshlrev_b32_e32 v14, 3, v11
	s_lshl_b64 s[2:3], s[0:1], 2
	v_lshlrev_b32_e32 v7, 5, v6
	v_lshl_or_b32 v9, v5, 1, v8
	v_lshl_or_b32 v14, v10, 6, v14
	v_lshlrev_b32_e32 v15, 2, v12
	s_add_u32 s24, s4, s2
	v_lshlrev_b32_e32 v13, 16, v9
	v_or3_b32 v14, v14, v15, v7
	s_addc_u32 s1, s5, s3
	v_lshl_or_b32 v222, v14, 2, v13
	s_and_b32 s25, s1, 0xffff
	s_movk_i32 s1, 0x2000
	buffer_load_dwordx4 v[110:113], v222, s[24:27], 0 offen
	buffer_load_dwordx4 v[114:117], v222, s[24:27], s66 offen
	s_mov_b32 s2, 0x8000
	buffer_load_dwordx4 v[122:125], v222, s[24:27], s1 offen
	buffer_load_dwordx4 v[118:121], v222, s[24:27], s2 offen
	s_movk_i32 s1, 0x4000
	s_mov_b32 s2, 0xa000
	buffer_load_dwordx4 v[126:129], v222, s[24:27], s1 offen
	buffer_load_dwordx4 v[130:133], v222, s[24:27], s2 offen
	s_mov_b32 s1, 0xc000
	s_mov_b32 s2, 0xe000
	buffer_load_dwordx4 v[138:141], v222, s[24:27], s1 offen
	buffer_load_dwordx4 v[142:145], v222, s[24:27], s2 offen
	s_waitcnt vmcnt(8)
	v_cmp_ne_u32_e32 vcc, -1, v214
	s_and_saveexec_b64 vcc, vcc
	v_ashrrev_i32_e32 v17, 31, v214
	v_mov_b32_e32 v16, v214
	v_lshl_add_u64 v[16:17], v[16:17], 2, s[56:57]
	global_load_dword v215, v[16:17], off
	s_or_b64 exec, exec, vcc
	v_lshlrev_b32_e32 v16, 3, v3
	v_and_b32_e32 v13, 63, v3
	v_lshlrev_b32_e32 v8, 4, v8
	v_and_b32_e32 v17, 24, v16
	v_bitop3_b32 v7, v8, v7, v17 bitop3:0xde
	v_lshlrev_b32_e32 v8, 4, v13
	v_lshl_or_b32 v230, v4, 10, v8
	v_lshlrev_b32_e32 v8, 2, v10
	v_lshlrev_b32_e32 v6, 1, v6
	v_or3_b32 v6, v8, v6, v12
	v_lshlrev_b32_e32 v8, 2, v3
	v_and_b32_e32 v10, 0xfffffc00, v8
	v_lshl_add_u32 v6, v6, 11, v10
	v_lshlrev_b32_e32 v10, 8, v11
	v_lshlrev_b32_e32 v9, 4, v9
	v_and_b32_e32 v15, 15, v3
	v_and_or_b32 v9, v9, 48, v10
	v_and_b32_e32 v10, 32, v16
	v_bitop3_b32 v220, v6, v9, v10 bitop3:0xf6
	v_lshlrev_b32_e32 v6, 6, v15
	v_and_b32_e32 v9, 48, v3
	v_and_b32_e32 v8, 32, v8
	v_or_b32_e32 v10, v6, v9
	v_bitop3_b32 v6, v6, v8, v9 bitop3:0x36
	v_lshlrev_b32_e32 v4, 13, v4
	v_ashrrev_i32_e32 v14, 8, v3
	v_and_or_b32 v227, v4, s66, v6
	v_lshlrev_b32_e32 v4, 16, v5
	v_lshlrev_b32_e32 v3, 10, v3
	s_mov_b32 s1, 0xf000
	v_lshlrev_b32_e32 v219, 6, v12
	v_and_or_b32 v3, v3, s1, v4
	v_lshlrev_b32_e32 v9, 14, v14
	v_lshl_or_b32 v225, v7, 1, v3
	v_cmp_eq_u32_e32 vcc, 0, v216
	v_add_u32_e32 v228, 0, v220
	v_add_u32_e32 v3, 0xc0, v219
	v_bitop3_b32 v217, v10, v9, v8 bitop3:0xde
	v_or_b32_e32 v218, 0x8000, v227
	v_readfirstlane_b32 s1, v14
	v_add_u32_e32 v226, 0x40000, v225
	v_add_u32_e32 v224, 0x80000, v225
	v_add_u32_e32 v223, 0xc0000, v225
	v_add_u32_e32 v229, v228, v219
	v_and_b32_e32 v221, 0xc0, v3
	s_mov_b64 s[6:7], s[10:11]
	s_cbranch_vccnz .LBB0_1574
	s_sub_i32 s2, s83, s85
	s_mov_b32 s99, s2
	v_readfirstlane_b32 s100, v0
	s_nop 3
	s_lshr_b32 s100, s100, 7
	s_lshl_b32 s100, s100, 4
	s_add_i32 s2, s2, 15
	s_ashr_i32 s2, s2, 4
	s_cmp_eq_u32 s1, 0
	s_cselect_b32 s1, s2, 0
	v_readfirstlane_b32 s2, v230
	s_and_b32 s2, s2, 0xfffffc00
	s_add_i32 s2, s2, 0
	s_mov_b32 s38, s26
	s_mov_b32 s39, s27
	s_mov_b32 m0, s2
	s_waitcnt vmcnt(4)
	v_mov_b64_e32 v[4:5], v[118:119]
	buffer_load_dwordx4 v225, s[36:39], 0 offen lds
	s_add_i32 m0, s2, 0x2000
	s_waitcnt vmcnt(2)
	v_mov_b64_e32 v[8:9], v[138:139]
	buffer_load_dwordx4 v226, s[36:39], 0 offen lds
	s_add_i32 m0, s2, 0x4000
	v_mov_b64_e32 v[12:13], v[122:123]
	buffer_load_dwordx4 v224, s[36:39], 0 offen lds
	s_add_i32 m0, s2, 0x6000
	v_mov_b64_e32 v[16:17], v[114:115]
	v_mov_b64_e32 v[20:21], v[130:131]
	v_mov_b64_e32 v[24:25], v[110:111]
	s_waitcnt vmcnt(3)
	v_mov_b64_e32 v[28:29], v[142:143]
	v_mov_b64_e32 v[32:33], v[126:127]
	buffer_load_dwordx4 v223, s[36:39], 0 offen lds
	v_mov_b64_e32 v[6:7], v[120:121]
	v_mov_b64_e32 v[10:11], v[140:141]
	v_mov_b64_e32 v[14:15], v[124:125]
	v_mov_b64_e32 v[18:19], v[116:117]
	v_mov_b64_e32 v[22:23], v[132:133]
	v_mov_b64_e32 v[26:27], v[112:113]
	v_mov_b64_e32 v[30:31], v[144:145]
	v_mov_b64_e32 v[34:35], v[128:129]
	s_waitcnt vmcnt(0)
	s_movk_i32 s101, 0x80
	s_cmp_le_i32 s99, s100
	s_cbranch_scc1 .Lmy_rcdP0
	buffer_load_dwordx4 v[236:239], v225, s[36:39], s101 offen
; #define G_DMA_A(buf, t, i_) __builtin_amdgcn_raw_ptr_buffer_load_lds(ra, (LAS void*)(lds + (buf) * 65536 + a_wu + (i_) * 8192), 16, ao##i_, (unsigned)(t) * 128u, 0, 0)
; #define G_ISSUE_B(t) do { const unsigned so_ = (unsigned)(t) * 64u * ldbB; _Pragma("unroll") for (int i_ = 0; i_ < 8; ++i_) sb[i_] = __builtin_bit_cast(f32x4, __builtin_amdgcn_raw_buffer_load_b128(rb, bo, so_ + (unsigned)i_ * ldbB, 0)); } while (0)
; #define G_RETIRE() asm volatile("s_waitcnt vmcnt(0)" : "+v"(sb[0]), "+v"(sb[1]), "+v"(sb[2]), "+v"(sb[3]), "+v"(sb[4]), "+v"(sb[5]), "+v"(sb[6]), "+v"(sb[7]) :: "memory")
; #define G_WRITE_B(buf) do { LAS unsigned char* d_ = lds + (buf) * 65536; \
;         _Pragma("unroll") for (int j_ = 0; j_ < 4; ++j_) { u32x4 w_; w_.x = cvtpk(sb[0][j_], sb[1][j_]); w_.y = cvtpk(sb[2][j_], sb[3][j_]); w_.z = cvtpk(sb[4][j_], sb[5][j_]); w_.w = cvtpk(sb[6][j_], sb[7][j_]); \
;             *(LAS u32x4*)(d_ + 32768 + T.b_w + ((T.b_rot + 64u * j_) & 255u)) = w_; } } while (0)
; #define G_BAR() do { asm volatile("s_waitcnt lgkmcnt(0)" ::: "memory"); __builtin_amdgcn_s_barrier(); asm volatile("" ::: "memory"); } while (0)
; #define G_DMA_A(buf, t, i_) __builtin_amdgcn_raw_ptr_buffer_load_lds(ra, (LAS void*)(lds + (buf) * 65536 + a_wu + (i_) * 8192), 16, ao##i_, (unsigned)(t) * 128u, 0, 0)
; #define G_ISSUE_B(t) do { const unsigned so_ = (unsigned)(t) * 64u * ldbB; _Pragma("unroll") for (int i_ = 0; i_ < 8; ++i_) sb[i_] = __builtin_bit_cast(f32x4, __builtin_amdgcn_raw_buffer_load_b128(rb, bo, so_ + (unsigned)i_ * ldbB, 0)); } while (0)
; #define G_RETIRE() asm volatile("s_waitcnt vmcnt(0)" : "+v"(sb[0]), "+v"(sb[1]), "+v"(sb[2]), "+v"(sb[3]), "+v"(sb[4]), "+v"(sb[5]), "+v"(sb[6]), "+v"(sb[7]) :: "memory")
; __device__ __forceinline__ void gemm_kloop_light(f32x4 (&acc)[8][4], LAS unsigned char* lds, const GemmT& T, ...
;     ...
;     G_ISSUE_B(0); G_DMA_A(0, 0, 0); G_DMA_A(0, 0, 1); G_DMA_A(0, 0, 2); G_DMA_A(0, 0, 3); G_RETIRE(); G_WRITE_B(0);
;     if (nt > 1) G_ISSUE_B(1);
;     G_BAR();
;     ...
;         if (w1) { G_RETIRE(); G_WRITE_B(cur ^ 1); }
;         if (i2) G_ISSUE_B(t + 2);
.Lmy_rcdP0:
	s_cmp_lt_i32 s99, 65
	s_cbranch_scc1 .Lmy_rcdP1
	buffer_load_dwordx4 v[240:243], v226, s[36:39], s101 offen
.Lmy_rcdP1:
	buffer_load_dwordx4 v[162:165], v222, s[24:27], s67 offen
	buffer_load_dwordx4 v[170:173], v222, s[24:27], s68 offen
	buffer_load_dwordx4 v[174:177], v222, s[24:27], s69 offen
	buffer_load_dwordx4 v[178:181], v222, s[24:27], s70 offen
	buffer_load_dwordx4 v[182:185], v222, s[24:27], s71 offen
	buffer_load_dwordx4 v[186:189], v222, s[24:27], s76 offen
	buffer_load_dwordx4 v[190:193], v222, s[24:27], s77 offen
	buffer_load_dwordx4 v[194:197], v222, s[24:27], s78 offen
	s_cmp_gt_i32 s1, 0
	s_cselect_b64 s[60:61], -1, 0
	s_cmp_lg_u32 s1, 1
	v_cvt_pk_bf16_f32 v36, v24, v12
	v_cvt_pk_bf16_f32 v37, v32, v16
	v_cvt_pk_bf16_f32 v38, v4, v20
	v_cvt_pk_bf16_f32 v39, v8, v28
	s_cselect_b64 s[58:59], -1, 0
	s_cmp_gt_i32 s1, 2
	ds_write_b128 v229, v[36:39] offset:32768
	v_cvt_pk_bf16_f32 v36, v25, v13
	v_cvt_pk_bf16_f32 v37, v33, v17
	v_cvt_pk_bf16_f32 v38, v5, v21
	v_cvt_pk_bf16_f32 v39, v9, v29
	s_cselect_b64 s[54:55], -1, 0
	s_cmp_gt_i32 s1, 3
	ds_write_b128 v229, v[36:39] offset:32832
	v_cvt_pk_bf16_f32 v36, v26, v14
	v_cvt_pk_bf16_f32 v37, v34, v18
	v_cvt_pk_bf16_f32 v38, v6, v22
	v_cvt_pk_bf16_f32 v39, v10, v30
	v_cvt_pk_bf16_f32 v4, v27, v15
	v_cvt_pk_bf16_f32 v5, v35, v19
	v_cvt_pk_bf16_f32 v6, v7, v23
	v_cvt_pk_bf16_f32 v7, v11, v31
	v_add_u32_e32 v3, v228, v221
	s_cselect_b64 s[50:51], -1, 0
	s_cmp_gt_i32 s1, 4
	ds_write_b128 v229, v[36:39] offset:32896
	ds_write_b128 v3, v[4:7] offset:32768
	s_cselect_b64 s[48:49], -1, 0
	s_cmp_gt_i32 s1, 5
	s_waitcnt lgkmcnt(0)
	s_barrier
	s_cselect_b64 s[46:47], -1, 0
	s_cmp_gt_i32 s1, 6
	v_mov_b32_e32 v4, v2
	v_mov_b32_e32 v5, v2
	s_cselect_b64 s[44:45], -1, 0
	s_cmp_gt_i32 s1, 7
	v_mov_b32_e32 v3, v2
	v_mov_b64_e32 v[12:13], v[4:5]
	v_mov_b64_e32 v[8:9], v[4:5]
	v_mov_b64_e32 v[20:21], v[4:5]
	v_mov_b64_e32 v[16:17], v[4:5]
	v_mov_b64_e32 v[28:29], v[4:5]
	v_mov_b64_e32 v[24:25], v[4:5]
	v_mov_b64_e32 v[36:37], v[4:5]
	v_mov_b64_e32 v[32:33], v[4:5]
	v_mov_b64_e32 v[44:45], v[4:5]
	v_mov_b64_e32 v[40:41], v[4:5]
	v_mov_b64_e32 v[52:53], v[4:5]
	v_mov_b64_e32 v[48:49], v[4:5]
	v_mov_b64_e32 v[60:61], v[4:5]
	v_mov_b64_e32 v[56:57], v[4:5]
	v_mov_b64_e32 v[68:69], v[4:5]
	v_mov_b64_e32 v[64:65], v[4:5]
	v_mov_b64_e32 v[76:77], v[4:5]
	v_mov_b64_e32 v[72:73], v[4:5]
	v_mov_b64_e32 v[84:85], v[4:5]
	v_mov_b64_e32 v[80:81], v[4:5]
	v_mov_b64_e32 v[92:93], v[4:5]
	v_mov_b64_e32 v[88:89], v[4:5]
	v_mov_b64_e32 v[100:101], v[4:5]
	v_mov_b64_e32 v[96:97], v[4:5]
	v_mov_b64_e32 v[108:109], v[4:5]
	v_mov_b64_e32 v[104:105], v[4:5]
	v_mov_b64_e32 v[148:149], v[4:5]
	v_mov_b64_e32 v[136:137], v[4:5]
	v_mov_b64_e32 v[156:157], v[4:5]
	v_mov_b64_e32 v[152:153], v[4:5]
	v_mov_b64_e32 v[168:169], v[4:5]
	v_mov_b64_e32 v[160:161], v[4:5]
	s_mov_b32 s3, 0
	s_cselect_b64 s[34:35], -1, 0
	s_mov_b32 s72, 0x10e000
	s_movk_i32 s73, 0x80
	v_mov_b64_e32 v[10:11], v[2:3]
	v_mov_b64_e32 v[6:7], v[2:3]
	v_mov_b64_e32 v[18:19], v[2:3]
	v_mov_b64_e32 v[14:15], v[2:3]
	v_mov_b64_e32 v[26:27], v[2:3]
	v_mov_b64_e32 v[22:23], v[2:3]
	v_mov_b64_e32 v[34:35], v[2:3]
	v_mov_b64_e32 v[30:31], v[2:3]
	v_mov_b64_e32 v[42:43], v[2:3]
	v_mov_b64_e32 v[38:39], v[2:3]
	v_mov_b64_e32 v[50:51], v[2:3]
	v_mov_b64_e32 v[46:47], v[2:3]
	v_mov_b64_e32 v[58:59], v[2:3]
	v_mov_b64_e32 v[54:55], v[2:3]
	v_mov_b64_e32 v[66:67], v[2:3]
	v_mov_b64_e32 v[62:63], v[2:3]
	v_mov_b64_e32 v[74:75], v[2:3]
	v_mov_b64_e32 v[70:71], v[2:3]
	v_mov_b64_e32 v[82:83], v[2:3]
	v_mov_b64_e32 v[78:79], v[2:3]
	v_mov_b64_e32 v[90:91], v[2:3]
	v_mov_b64_e32 v[86:87], v[2:3]
	v_mov_b64_e32 v[98:99], v[2:3]
	v_mov_b64_e32 v[94:95], v[2:3]
	v_mov_b64_e32 v[106:107], v[2:3]
	v_mov_b64_e32 v[102:103], v[2:3]
	v_mov_b64_e32 v[146:147], v[2:3]
	v_mov_b64_e32 v[134:135], v[2:3]
	v_mov_b64_e32 v[154:155], v[2:3]
	v_mov_b64_e32 v[150:151], v[2:3]
	v_mov_b64_e32 v[166:167], v[2:3]
	v_mov_b64_e32 v[158:159], v[2:3]
	s_cmp_ge_i32 s100, 32
	s_cbranch_scc0 .Lmy_d2d_nopre
	s_mov_b32 s98, 0x10e000
	s_add_i32 s6, s98, 0xffff2000
	buffer_load_dwordx4 v[8:11], v222, s[24:27], s6 offen
	s_add_i32 s7, s98, 0xffff4000
	buffer_load_dwordx4 v[12:15], v222, s[24:27], s7 offen
	s_add_i32 s6, s98, 0xffff6000
	buffer_load_dwordx4 v[16:19], v222, s[24:27], s6 offen
	s_add_i32 s7, s98, 0xffff8000
	buffer_load_dwordx4 v[20:23], v222, s[24:27], s7 offen
	s_add_i32 s6, s98, 0xffffa000
	buffer_load_dwordx4 v[24:27], v222, s[24:27], s6 offen
	s_add_i32 s7, s98, 0xffffc000
	buffer_load_dwordx4 v[28:31], v222, s[24:27], s7 offen
	s_add_i32 s6, s98, 0xffffe000
	buffer_load_dwordx4 v[32:35], v222, s[24:27], s6 offen
	buffer_load_dwordx4 v[36:39], v222, s[24:27], s98 offen

; #define G_ISSUE_B(t) do { const unsigned so_ = (unsigned)(t) * 64u * ldbB; _Pragma("unroll") for (int i_ = 0; i_ < 8; ++i_) sb[i_] = __builtin_bit_cast(f32x4, __builtin_amdgcn_raw_buffer_load_b128(rb, bo, so_ + (unsigned)i_ * ldbB, 0)); } while (0)
; #define G_RETIRE() asm volatile("s_waitcnt vmcnt(0)" : "+v"(sb[0]), "+v"(sb[1]), "+v"(sb[2]), "+v"(sb[3]), "+v"(sb[4]), "+v"(sb[5]), "+v"(sb[6]), "+v"(sb[7]) :: "memory")
; #define G_WRITE_B(buf) do { LAS unsigned char* d_ = lds + (buf) * 65536; \
;         _Pragma("unroll") for (int j_ = 0; j_ < 4; ++j_) { u32x4 w_; w_.x = cvtpk(sb[0][j_], sb[1][j_]); w_.y = cvtpk(sb[2][j_], sb[3][j_]); w_.z = cvtpk(sb[4][j_], sb[5][j_]); w_.w = cvtpk(sb[6][j_], sb[7][j_]); \
;             *(LAS u32x4*)(d_ + 32768 + T.b_w + ((T.b_rot + 64u * j_) & 255u)) = w_; } } while (0)
; #define G_ISSUE_B(t) do { const unsigned so_ = (unsigned)(t) * 64u * ldbB; _Pragma("unroll") for (int i_ = 0; i_ < 8; ++i_) sb[i_] = __builtin_bit_cast(f32x4, __builtin_amdgcn_raw_buffer_load_b128(rb, bo, so_ + (unsigned)i_ * ldbB, 0)); } while (0)
; #define G_RETIRE() asm volatile("s_waitcnt vmcnt(0)" : "+v"(sb[0]), "+v"(sb[1]), "+v"(sb[2]), "+v"(sb[3]), "+v"(sb[4]), "+v"(sb[5]), "+v"(sb[6]), "+v"(sb[7]) :: "memory")
; #define G_WRITE_B(buf) do { LAS unsigned char* d_ = lds + (buf) * 65536; \
;         _Pragma("unroll") for (int j_ = 0; j_ < 4; ++j_) { u32x4 w_; w_.x = cvtpk(sb[0][j_], sb[1][j_]); w_.y = cvtpk(sb[2][j_], sb[3][j_]); w_.z = cvtpk(sb[4][j_], sb[5][j_]); w_.w = cvtpk(sb[6][j_], sb[7][j_]); \
;             *(LAS u32x4*)(d_ + 32768 + T.b_w + ((T.b_rot + 64u * j_) & 255u)) = w_; } } while (0)
; __device__ __forceinline__ void gemm_kloop_light(f32x4 (&acc)[8][4], LAS unsigned char* lds, const GemmT& T, ...
;     ...
;         if (w1) { G_RETIRE(); G_WRITE_B(cur ^ 1); }
;         if (i2) G_ISSUE_B(t + 2);
.LBB0_1485:
	s_cmp_ge_i32 s100, 32
	s_cbranch_scc1 .Lmy_d2d_s47
	s_waitcnt vmcnt(0)
	v_add_u32_e32 v244, s74, v230
	s_add_i32 s101, s73, 0x80
	s_cmp_le_i32 s99, s100
	s_cbranch_scc1 .Lmy_rcdL0
	ds_write_b128 v244, v[236:239]
	buffer_load_dwordx4 v[236:239], v225, s[36:39], s101 offen
.Lmy_rcdL0:
	s_cmp_lt_i32 s99, 65
	s_cbranch_scc1 .Lmy_rcdL1
	ds_write_b128 v244, v[240:243] offset:8192
	buffer_load_dwordx4 v[240:243], v226, s[36:39], s101 offen
.Lmy_rcdL1:
	s_add_i32 s6, s72, 0xffff2000
	v_cvt_pk_bf16_f32 v198, v162, v170
	v_cvt_pk_bf16_f32 v202, v163, v171
	v_cvt_pk_bf16_f32 v206, v164, v172
	v_cvt_pk_bf16_f32 v210, v165, v173
	s_add_i32 s7, s72, 0xffff4000
	buffer_load_dwordx4 v[162:165], v222, s[24:27], s6 offen
	buffer_load_dwordx4 v[170:173], v222, s[24:27], s7 offen
	s_add_i32 s6, s72, 0xffff6000
	v_cvt_pk_bf16_f32 v199, v174, v178
	v_cvt_pk_bf16_f32 v203, v175, v179
	v_cvt_pk_bf16_f32 v207, v176, v180
	v_cvt_pk_bf16_f32 v211, v177, v181
	s_add_i32 s7, s72, 0xffff8000
	buffer_load_dwordx4 v[174:177], v222, s[24:27], s6 offen
	buffer_load_dwordx4 v[178:181], v222, s[24:27], s7 offen
	s_add_i32 s6, s72, 0xffffa000
	v_cvt_pk_bf16_f32 v200, v182, v186
	v_cvt_pk_bf16_f32 v204, v183, v187
	v_cvt_pk_bf16_f32 v208, v184, v188
	v_cvt_pk_bf16_f32 v212, v185, v189
	s_add_i32 s7, s72, 0xffffc000
	buffer_load_dwordx4 v[182:185], v222, s[24:27], s6 offen
	buffer_load_dwordx4 v[186:189], v222, s[24:27], s7 offen
	s_add_i32 s6, s72, 0xffffe000
	v_cvt_pk_bf16_f32 v201, v190, v194
	v_cvt_pk_bf16_f32 v205, v191, v195
	v_cvt_pk_bf16_f32 v209, v192, v196
	v_cvt_pk_bf16_f32 v213, v193, v197
	buffer_load_dwordx4 v[190:193], v222, s[24:27], s6 offen
	buffer_load_dwordx4 v[194:197], v222, s[24:27], s72 offen
	s_branch .Lmy_d2d_wr
.Lmy_d2d_s47:
	s_waitcnt vmcnt(8)
	v_add_u32_e32 v244, s74, v230
	s_add_i32 s101, s73, 0x80
	s_cmp_le_i32 s99, s100
	s_cbranch_scc1 .Lmy_rcdM0
	ds_write_b128 v244, v[236:239]
	buffer_load_dwordx4 v[236:239], v225, s[36:39], s101 offen

; #define LAS __attribute__((address_space(3)))
; #define G_DMA_A(buf, t, i_) __builtin_amdgcn_raw_ptr_buffer_load_lds(ra, (LAS void*)(lds + (buf) * 65536 + a_wu + (i_) * 8192), 16, ao##i_, (unsigned)(t) * 128u, 0, 0)
; #define G_ISSUE_B(t) do { const unsigned so_ = (unsigned)(t) * 64u * ldbB; _Pragma("unroll") for (int i_ = 0; i_ < 8; ++i_) sb[i_] = __builtin_bit_cast(f32x4, __builtin_amdgcn_raw_buffer_load_b128(rb, bo, so_ + (unsigned)i_ * ldbB, 0)); } while (0)
; #define G_RETIRE() asm volatile("s_waitcnt vmcnt(0)" : "+v"(sb[0]), "+v"(sb[1]), "+v"(sb[2]), "+v"(sb[3]), "+v"(sb[4]), "+v"(sb[5]), "+v"(sb[6]), "+v"(sb[7]) :: "memory")
; #define G_WRITE_B(buf) do { LAS unsigned char* d_ = lds + (buf) * 65536; \
;         _Pragma("unroll") for (int j_ = 0; j_ < 4; ++j_) { u32x4 w_; w_.x = cvtpk(sb[0][j_], sb[1][j_]); w_.y = cvtpk(sb[2][j_], sb[3][j_]); w_.z = cvtpk(sb[4][j_], sb[5][j_]); w_.w = cvtpk(sb[6][j_], sb[7][j_]); \
;             *(LAS u32x4*)(d_ + 32768 + T.b_w + ((T.b_rot + 64u * j_) & 255u)) = w_; } } while (0)
; #define G_DMA_A(buf, t, i_) __builtin_amdgcn_raw_ptr_buffer_load_lds(ra, (LAS void*)(lds + (buf) * 65536 + a_wu + (i_) * 8192), 16, ao##i_, (unsigned)(t) * 128u, 0, 0)
; __device__ __forceinline__ void gemm_kloop_light(f32x4 (&acc)[8][4], LAS unsigned char* lds, const GemmT& T, ...
;     ...
;     for (int t = 0; t < nt; ++t) { const int cur = t & 1; const bool w1 = t + 1 < nt, i2 = t + 2 < nt;
;         if (w1) { G_DMA_A(cur ^ 1, t + 1, 0); G_DMA_A(cur ^ 1, t + 1, 1); G_DMA_A(cur ^ 1, t + 1, 2); G_DMA_A(cur ^ 1, t + 1, 3); }
;         if (mlim > 0) {
; #pragma unroll
;             for (int ks = 0; ks < 2; ++ks) { const LAS unsigned char* s_ = lds + cur * 65536 + ks * 1024; bf16x8 Bf_[4];
; #pragma unroll
;                 for (int n_ = 0; n_ < 4; ++n_) Bf_[n_] = *(const LAS bf16x8*)(s_ + T.b_r + n_ * 2048);
; #pragma unroll
;                 for (int m_ = 0; m_ < 8; ++m_) if (m_ < mlim) { const bf16x8 At_ = *(const LAS bf16x8*)(s_ + T.a_r + m_ * 2048);
; #pragma unroll
;                     for (int n_ = 0; n_ < 4; ++n_) acc[m_][n_] = __builtin_amdgcn_mfma_f32_16x16x32_bf16(Bf_[n_], At_, acc[m_][n_], 0, 0, 0); } } }
;         if (w1) { G_RETIRE(); G_WRITE_B(cur ^ 1); }
;         if (i2) G_ISSUE_B(t + 2);
.Lmy_rcdM1:
	s_bitcmp1_b32 s3, 16
	s_cbranch_scc1 .Lmy_d2d_odd
	v_cvt_pk_bf16_f32 v198, v162, v170
	v_cvt_pk_bf16_f32 v199, v174, v178
	v_cvt_pk_bf16_f32 v200, v182, v186
	v_cvt_pk_bf16_f32 v201, v190, v194
	v_cvt_pk_bf16_f32 v202, v163, v171
	v_cvt_pk_bf16_f32 v203, v175, v179
	v_cvt_pk_bf16_f32 v204, v183, v187
	v_cvt_pk_bf16_f32 v205, v191, v195
	v_cvt_pk_bf16_f32 v206, v164, v172
	v_cvt_pk_bf16_f32 v207, v176, v180
	v_cvt_pk_bf16_f32 v208, v184, v188
	v_cvt_pk_bf16_f32 v209, v192, v196
	v_cvt_pk_bf16_f32 v210, v165, v173
	v_cvt_pk_bf16_f32 v211, v177, v181
	v_cvt_pk_bf16_f32 v212, v185, v189
	v_cvt_pk_bf16_f32 v213, v193, v197
	s_cmp_gt_u32 s72, 0xf0e000
	s_cbranch_scc1 .Lmy_d2d_wr
	s_add_i32 s6, s72, 0x72000
	buffer_load_dwordx4 v[162:165], v222, s[24:27], s6 offen
	s_add_i32 s7, s72, 0x74000
	buffer_load_dwordx4 v[170:173], v222, s[24:27], s7 offen
	s_add_i32 s6, s72, 0x76000
	buffer_load_dwordx4 v[174:177], v222, s[24:27], s6 offen
	s_add_i32 s7, s72, 0x78000
	buffer_load_dwordx4 v[178:181], v222, s[24:27], s7 offen
	s_add_i32 s6, s72, 0x7a000
	buffer_load_dwordx4 v[182:185], v222, s[24:27], s6 offen
	s_add_i32 s7, s72, 0x7c000
	buffer_load_dwordx4 v[186:189], v222, s[24:27], s7 offen
	s_add_i32 s6, s72, 0x7e000
	buffer_load_dwordx4 v[190:193], v222, s[24:27], s6 offen
	s_add_i32 s7, s72, 0x80000
	buffer_load_dwordx4 v[194:197], v222, s[24:27], s7 offen
	s_branch .Lmy_d2d_wr
.Lmy_d2d_odd:
	v_cvt_pk_bf16_f32 v198, v8, v12
	v_cvt_pk_bf16_f32 v199, v16, v20
	v_cvt_pk_bf16_f32 v200, v24, v28
	v_cvt_pk_bf16_f32 v201, v32, v36
	v_cvt_pk_bf16_f32 v202, v9, v13
	v_cvt_pk_bf16_f32 v203, v17, v21
	v_cvt_pk_bf16_f32 v204, v25, v29
	v_cvt_pk_bf16_f32 v205, v33, v37
	v_cvt_pk_bf16_f32 v206, v10, v14
	v_cvt_pk_bf16_f32 v207, v18, v22
	v_cvt_pk_bf16_f32 v208, v26, v30
	v_cvt_pk_bf16_f32 v209, v34, v38
	v_cvt_pk_bf16_f32 v210, v11, v15
	v_cvt_pk_bf16_f32 v211, v19, v23
	v_cvt_pk_bf16_f32 v212, v27, v31
	v_cvt_pk_bf16_f32 v213, v35, v39
	s_cmp_gt_u32 s72, 0xf0e000
	s_cbranch_scc1 .Lmy_d2d_wr
	s_add_i32 s6, s72, 0x72000
	buffer_load_dwordx4 v[8:11], v222, s[24:27], s6 offen
	s_add_i32 s7, s72, 0x74000
	buffer_load_dwordx4 v[12:15], v222, s[24:27], s7 offen
	s_add_i32 s6, s72, 0x76000
	buffer_load_dwordx4 v[16:19], v222, s[24:27], s6 offen
	s_add_i32 s7, s72, 0x78000
	buffer_load_dwordx4 v[20:23], v222, s[24:27], s7 offen
	s_add_i32 s6, s72, 0x7a000
	buffer_load_dwordx4 v[24:27], v222, s[24:27], s6 offen
	s_add_i32 s7, s72, 0x7c000
	buffer_load_dwordx4 v[28:31], v222, s[24:27], s7 offen
	s_add_i32 s6, s72, 0x7e000
	buffer_load_dwordx4 v[32:35], v222, s[24:27], s6 offen
	s_add_i32 s7, s72, 0x80000
	buffer_load_dwordx4 v[36:39], v222, s[24:27], s7 offen
.Lmy_d2d_wr:
	v_add_u32_e32 v3, s74, v228
	v_add_u32_e32 v4, v3, v219
	v_add_u32_e32 v3, v3, v221
	ds_write_b128 v4, v[198:201] offset:32768
	ds_write_b128 v4, v[202:205] offset:32832
	ds_write_b128 v4, v[206:209] offset:32896
	ds_write_b128 v3, v[210:213] offset:32768
	s_waitcnt lgkmcnt(0)
	s_barrier
	s_add_i32 s72, s72, 0x80000
	s_add_i32 s3, s3, 0x10000
	s_addk_i32 s73, 0x80
	s_cmp_eq_u32 s72, 0x100e000
	s_cbranch_scc1 .LBB0_1515
.LBB0_1486:
	s_and_b32 s6, s3, 0x10000
	s_xor_b32 s74, s6, 0x10000
	v_cndmask_b32_e64 v3, 0, 1, s[60:61]
	s_andn2_b64 vcc, exec, s[60:61]
	v_cmp_ne_u32_e64 s[4:5], 1, v3
	s_cbranch_vccnz .LBB0_1485
	s_add_i32 s6, s6, 0
	v_add_u32_e32 v4, s6, v227
	ds_read_b128 v[198:201], v4 offset:32768
	v_add_u32_e32 v3, s6, v217
	ds_read_b128 v[202:205], v4 offset:34816
	ds_read_b128 v[232:235], v3
	ds_read_b128 v[206:209], v4 offset:36864
	ds_read_b128 v[210:213], v4 offset:38912
	s_waitcnt lgkmcnt(2)
	v_mfma_f32_16x16x32_bf16 v[166:169], v[202:205], v[232:235], v[166:169]
	v_cndmask_b32_e64 v5, 0, 1, s[58:59]
	v_cmp_ne_u32_e64 s[6:7], 1, v5
	s_andn2_b64 vcc, exec, s[58:59]
	v_mfma_f32_16x16x32_bf16 v[158:161], v[198:201], v[232:235], v[158:161]
	s_waitcnt lgkmcnt(1)
	v_mfma_f32_16x16x32_bf16 v[150:153], v[206:209], v[232:235], v[150:153]
	s_waitcnt lgkmcnt(0)
	v_mfma_f32_16x16x32_bf16 v[154:157], v[210:213], v[232:235], v[154:157]
	s_cbranch_vccnz .LBB0_1502
	ds_read_b128 v[232:235], v3 offset:2048
	s_waitcnt lgkmcnt(0)
	v_mfma_f32_16x16x32_bf16 v[134:137], v[198:201], v[232:235], v[134:137]
	v_mfma_f32_16x16x32_bf16 v[146:149], v[202:205], v[232:235], v[146:149]
	v_mfma_f32_16x16x32_bf16 v[102:105], v[206:209], v[232:235], v[102:105]
	v_mfma_f32_16x16x32_bf16 v[106:109], v[210:213], v[232:235], v[106:109]
	v_cndmask_b32_e64 v5, 0, 1, s[54:55]
	v_cmp_ne_u32_e64 s[8:9], 1, v5
	s_andn2_b64 vcc, exec, s[54:55]
	s_cbranch_vccz .LBB0_1503

; #define LAS __attribute__((address_space(3)))
; #define G_DMA_A(buf, t, i_) __builtin_amdgcn_raw_ptr_buffer_load_lds(ra, (LAS void*)(lds + (buf) * 65536 + a_wu + (i_) * 8192), 16, ao##i_, (unsigned)(t) * 128u, 0, 0)
; #define G_DMA_A(buf, t, i_) __builtin_amdgcn_raw_ptr_buffer_load_lds(ra, (LAS void*)(lds + (buf) * 65536 + a_wu + (i_) * 8192), 16, ao##i_, (unsigned)(t) * 128u, 0, 0)
; __device__ __forceinline__ void gemm_kloop_light(f32x4 (&acc)[8][4], LAS unsigned char* lds, const GemmT& T, ...
;     ...
;     for (int t = 0; t < nt; ++t) { const int cur = t & 1; const bool w1 = t + 1 < nt, i2 = t + 2 < nt;
;         if (w1) { G_DMA_A(cur ^ 1, t + 1, 0); G_DMA_A(cur ^ 1, t + 1, 1); G_DMA_A(cur ^ 1, t + 1, 2); G_DMA_A(cur ^ 1, t + 1, 3); }
;         if (mlim > 0) {
; #pragma unroll
;             for (int ks = 0; ks < 2; ++ks) { const LAS unsigned char* s_ = lds + cur * 65536 + ks * 1024; bf16x8 Bf_[4];
; #pragma unroll
;                 for (int n_ = 0; n_ < 4; ++n_) Bf_[n_] = *(const LAS bf16x8*)(s_ + T.b_r + n_ * 2048);
; #pragma unroll
;                 for (int m_ = 0; m_ < 8; ++m_) if (m_ < mlim) { const bf16x8 At_ = *(const LAS bf16x8*)(s_ + T.a_r + m_ * 2048);
; #pragma unroll
;                     for (int n_ = 0; n_ < 4; ++n_) acc[m_][n_] = __builtin_amdgcn_mfma_f32_16x16x32_bf16(Bf_[n_], At_, acc[m_][n_], 0, 0, 0); } } }
.LBB0_1515:
	s_add_i32 s3, s2, 0x16000
	s_add_i32 s6, s2, 0x14000
	s_add_i32 s2, s2, 0x12000
	s_mov_b32 s38, s26
	s_mov_b32 s39, s27
	v_cndmask_b32_e64 v3, 0, 1, s[58:59]
	s_and_b64 vcc, exec, s[4:5]
	v_cmp_ne_u32_e64 s[6:7], 1, v3
	s_cbranch_vccnz .LBB0_1532
	v_add_u32_e32 v4, 0, v227
	ds_read_b128 v[198:201], v4 offset:32768
	v_add_u32_e32 v3, 0, v217
	ds_read_b128 v[202:205], v4 offset:34816
	ds_read_b128 v[232:235], v3
	ds_read_b128 v[206:209], v4 offset:36864
	ds_read_b128 v[210:213], v4 offset:38912
	s_waitcnt lgkmcnt(2)
	v_mfma_f32_16x16x32_bf16 v[166:169], v[202:205], v[232:235], v[166:169]
	s_and_b64 vcc, exec, s[6:7]
	v_mfma_f32_16x16x32_bf16 v[158:161], v[198:201], v[232:235], v[158:161]
	s_waitcnt lgkmcnt(1)
	v_mfma_f32_16x16x32_bf16 v[150:153], v[206:209], v[232:235], v[150:153]
	s_waitcnt lgkmcnt(0)
	v_mfma_f32_16x16x32_bf16 v[154:157], v[210:213], v[232:235], v[154:157]
	s_cbranch_vccnz .LBB0_1550
	ds_read_b128 v[232:235], v3 offset:2048
	s_waitcnt lgkmcnt(0)
	v_mfma_f32_16x16x32_bf16 v[134:137], v[198:201], v[232:235], v[134:137]
	v_mfma_f32_16x16x32_bf16 v[146:149], v[202:205], v[232:235], v[146:149]
	v_mfma_f32_16x16x32_bf16 v[102:105], v[206:209], v[232:235], v[102:105]
	v_mfma_f32_16x16x32_bf16 v[106:109], v[210:213], v[232:235], v[106:109]
	v_cndmask_b32_e64 v5, 0, 1, s[54:55]
	v_cmp_ne_u32_e64 s[8:9], 1, v5
	s_andn2_b64 vcc, exec, s[54:55]
	s_cbranch_vccz .LBB0_1551

; #define G_ISSUE_B(t) do { const unsigned so_ = (unsigned)(t) * 64u * ldbB; _Pragma("unroll") for (int i_ = 0; i_ < 8; ++i_) sb[i_] = __builtin_bit_cast(f32x4, __builtin_amdgcn_raw_buffer_load_b128(rb, bo, so_ + (unsigned)i_ * ldbB, 0)); } while (0)
; #define G_RETIRE() asm volatile("s_waitcnt vmcnt(0)" : "+v"(sb[0]), "+v"(sb[1]), "+v"(sb[2]), "+v"(sb[3]), "+v"(sb[4]), "+v"(sb[5]), "+v"(sb[6]), "+v"(sb[7]) :: "memory")
; #define G_WRITE_B(buf) do { LAS unsigned char* d_ = lds + (buf) * 65536; \
;         _Pragma("unroll") for (int j_ = 0; j_ < 4; ++j_) { u32x4 w_; w_.x = cvtpk(sb[0][j_], sb[1][j_]); w_.y = cvtpk(sb[2][j_], sb[3][j_]); w_.z = cvtpk(sb[4][j_], sb[5][j_]); w_.w = cvtpk(sb[6][j_], sb[7][j_]); \
;             *(LAS u32x4*)(d_ + 32768 + T.b_w + ((T.b_rot + 64u * j_) & 255u)) = w_; } } while (0)
; #define G_ISSUE_B(t) do { const unsigned so_ = (unsigned)(t) * 64u * ldbB; _Pragma("unroll") for (int i_ = 0; i_ < 8; ++i_) sb[i_] = __builtin_bit_cast(f32x4, __builtin_amdgcn_raw_buffer_load_b128(rb, bo, so_ + (unsigned)i_ * ldbB, 0)); } while (0)
; #define G_RETIRE() asm volatile("s_waitcnt vmcnt(0)" : "+v"(sb[0]), "+v"(sb[1]), "+v"(sb[2]), "+v"(sb[3]), "+v"(sb[4]), "+v"(sb[5]), "+v"(sb[6]), "+v"(sb[7]) :: "memory")
; #define G_WRITE_B(buf) do { LAS unsigned char* d_ = lds + (buf) * 65536; \
;         _Pragma("unroll") for (int j_ = 0; j_ < 4; ++j_) { u32x4 w_; w_.x = cvtpk(sb[0][j_], sb[1][j_]); w_.y = cvtpk(sb[2][j_], sb[3][j_]); w_.z = cvtpk(sb[4][j_], sb[5][j_]); w_.w = cvtpk(sb[6][j_], sb[7][j_]); \
;             *(LAS u32x4*)(d_ + 32768 + T.b_w + ((T.b_rot + 64u * j_) & 255u)) = w_; } } while (0)
; __device__ __forceinline__ void gemm_kloop_light(f32x4 (&acc)[8][4], LAS unsigned char* lds, const GemmT& T, ...
;     ...
;         if (w1) { G_RETIRE(); G_WRITE_B(cur ^ 1); }
;         if (i2) G_ISSUE_B(t + 2);
.LBB0_1532:
	v_add_u32_e32 v3, s29, v220
	s_waitcnt vmcnt(4)
	s_waitcnt vmcnt(0)
	v_add_u32_e32 v244, 0x10000, v230
	s_cmp_le_i32 s99, s100
	s_cbranch_scc1 .Lmy_rcdT0
	ds_write_b128 v244, v[236:239]

; #define LAS __attribute__((address_space(3)))
; #define G_ISSUE_B(t) do { const unsigned so_ = (unsigned)(t) * 64u * ldbB; _Pragma("unroll") for (int i_ = 0; i_ < 8; ++i_) sb[i_] = __builtin_bit_cast(f32x4, __builtin_amdgcn_raw_buffer_load_b128(rb, bo, so_ + (unsigned)i_ * ldbB, 0)); } while (0)
; #define G_RETIRE() asm volatile("s_waitcnt vmcnt(0)" : "+v"(sb[0]), "+v"(sb[1]), "+v"(sb[2]), "+v"(sb[3]), "+v"(sb[4]), "+v"(sb[5]), "+v"(sb[6]), "+v"(sb[7]) :: "memory")
; #define G_WRITE_B(buf) do { LAS unsigned char* d_ = lds + (buf) * 65536; \
;         _Pragma("unroll") for (int j_ = 0; j_ < 4; ++j_) { u32x4 w_; w_.x = cvtpk(sb[0][j_], sb[1][j_]); w_.y = cvtpk(sb[2][j_], sb[3][j_]); w_.z = cvtpk(sb[4][j_], sb[5][j_]); w_.w = cvtpk(sb[6][j_], sb[7][j_]); \
;             *(LAS u32x4*)(d_ + 32768 + T.b_w + ((T.b_rot + 64u * j_) & 255u)) = w_; } } while (0)
; #define G_BAR() do { asm volatile("s_waitcnt lgkmcnt(0)" ::: "memory"); __builtin_amdgcn_s_barrier(); asm volatile("" ::: "memory"); } while (0)
; #define G_ISSUE_B(t) do { const unsigned so_ = (unsigned)(t) * 64u * ldbB; _Pragma("unroll") for (int i_ = 0; i_ < 8; ++i_) sb[i_] = __builtin_bit_cast(f32x4, __builtin_amdgcn_raw_buffer_load_b128(rb, bo, so_ + (unsigned)i_ * ldbB, 0)); } while (0)
; #define G_RETIRE() asm volatile("s_waitcnt vmcnt(0)" : "+v"(sb[0]), "+v"(sb[1]), "+v"(sb[2]), "+v"(sb[3]), "+v"(sb[4]), "+v"(sb[5]), "+v"(sb[6]), "+v"(sb[7]) :: "memory")
; __device__ __forceinline__ void gemm_kloop_light(f32x4 (&acc)[8][4], LAS unsigned char* lds, const GemmT& T, ...
;     ...
;             for (int ks = 0; ks < 2; ++ks) { const LAS unsigned char* s_ = lds + cur * 65536 + ks * 1024; bf16x8 Bf_[4];
; #pragma unroll
;                 for (int n_ = 0; n_ < 4; ++n_) Bf_[n_] = *(const LAS bf16x8*)(s_ + T.b_r + n_ * 2048);
; #pragma unroll
;                 for (int m_ = 0; m_ < 8; ++m_) if (m_ < mlim) { const bf16x8 At_ = *(const LAS bf16x8*)(s_ + T.a_r + m_ * 2048);
; #pragma unroll
;                     for (int n_ = 0; n_ < 4; ++n_) acc[m_][n_] = __builtin_amdgcn_mfma_f32_16x16x32_bf16(Bf_[n_], At_, acc[m_][n_], 0, 0, 0); } } }
;         if (w1) { G_RETIRE(); G_WRITE_B(cur ^ 1); }
;         if (i2) G_ISSUE_B(t + 2);
;         G_BAR(); }
.Lmy_rcdT1:
	v_add_u32_e32 v4, v3, v219
	v_cvt_pk_bf16_f32 v198, v162, v170
	v_cvt_pk_bf16_f32 v199, v174, v178
	v_cvt_pk_bf16_f32 v200, v182, v186
	v_cvt_pk_bf16_f32 v201, v190, v194
	ds_write_b128 v4, v[198:201]
	v_cvt_pk_bf16_f32 v198, v163, v171
	v_cvt_pk_bf16_f32 v199, v175, v179
	v_cvt_pk_bf16_f32 v200, v183, v187
	v_cvt_pk_bf16_f32 v201, v191, v195
	ds_write_b128 v4, v[198:201] offset:64
	v_cvt_pk_bf16_f32 v198, v164, v172
	v_cvt_pk_bf16_f32 v199, v176, v180
	v_cvt_pk_bf16_f32 v200, v184, v188
	v_cvt_pk_bf16_f32 v201, v192, v196
	v_cvt_pk_bf16_f32 v162, v165, v173
	v_cvt_pk_bf16_f32 v163, v177, v181
	v_cvt_pk_bf16_f32 v164, v185, v189
	v_cvt_pk_bf16_f32 v165, v193, v197
	v_add_u32_e32 v3, v3, v221
	ds_write_b128 v4, v[198:201] offset:128
	ds_write_b128 v3, v[162:165]
	s_waitcnt lgkmcnt(0)
	s_barrier
	s_and_b64 vcc, exec, s[4:5]
	s_cbranch_vccnz .LBB0_1549
	s_add_i32 s2, 0, 0x10000
	v_add_u32_e32 v4, s2, v218
	ds_read_b128 v[170:173], v4
	v_add_u32_e32 v3, s2, v217
	ds_read_b128 v[174:177], v4 offset:2048
	ds_read_b128 v[182:185], v3
	ds_read_b128 v[178:181], v4 offset:4096
	s_and_b64 vcc, exec, s[6:7]
	s_waitcnt lgkmcnt(1)
	v_mfma_f32_16x16x32_bf16 v[162:165], v[174:177], v[182:185], v[166:169]
	s_nop 2
	ds_read_b128 v[166:169], v4 offset:6144
	v_mfma_f32_16x16x32_bf16 v[158:161], v[170:173], v[182:185], v[158:161]
	s_waitcnt lgkmcnt(1)
	v_mfma_f32_16x16x32_bf16 v[150:153], v[178:181], v[182:185], v[150:153]
	s_waitcnt lgkmcnt(0)
	v_mfma_f32_16x16x32_bf16 v[154:157], v[166:169], v[182:185], v[154:157]
	s_cbranch_vccnz .LBB0_1562
	ds_read_b128 v[182:185], v3 offset:2048
	s_waitcnt lgkmcnt(0)
	v_mfma_f32_16x16x32_bf16 v[134:137], v[170:173], v[182:185], v[134:137]
	v_mfma_f32_16x16x32_bf16 v[146:149], v[174:177], v[182:185], v[146:149]
	v_mfma_f32_16x16x32_bf16 v[102:105], v[178:181], v[182:185], v[102:105]
	v_mfma_f32_16x16x32_bf16 v[106:109], v[166:169], v[182:185], v[106:109]
	s_cmp_gt_u32 s1, 2
	s_cselect_b64 s[4:5], -1, 0
	s_cmp_lt_u32 s1, 3
	s_cbranch_scc0 .LBB0_1563
